# P6 mid: min(1+exp(-gm), 2^20) replaces rcp/max/rcp; P9 epilogue (lin+1)*t as one fma; P5 rescale loop unrolled with the 7 later tiles' loads issued together before the barrier
# baseline (speedup 1.0000x reference)
.LBB0_790:
	s_lshl_b32 s96, s56, 1
	s_add_u32 s58, s42, s96
	s_addc_u32 s59, s43, 0
	v_mov_b32_e32 v143, v85
	v_mov_b64_e32 v[0:1], s[88:89]
	v_lshl_add_u64 v[10:11], s[58:59], 0, v[142:143]
	v_mad_u64_u32 v[0:1], s[58:59], v146, s65, v[0:1]
	v_mov_b32_e32 v2, v1
	v_mad_u64_u32 v[2:3], s[58:59], v147, s65, v[2:3]
	v_mov_b32_e32 v1, v2
	v_lshl_add_u64 v[0:1], v[0:1], 0, s[96:97]
	v_lshl_add_u64 v[0:1], v[0:1], 0, v[142:143]
	s_mov_b32 s49, s97
	v_lshl_add_u64 v[0:1], v[0:1], 0, s[48:49]
	v_lshl_add_u64 v[2:3], v[0:1], 0, s[50:51]
	v_add_co_u32_e32 v0, vcc, s73, v0
	s_lshl_b32 s56, s56, 2
	s_nop 0
	v_addc_co_u32_e32 v1, vcc, 0, v1, vcc
	global_load_dwordx2 v[22:23], v[0:1], off offset:2560
	global_load_dwordx2 v[16:17], v[2:3], off offset:32
	v_lshlrev_b64 v[0:1], 11, v[146:147]
	v_lshl_add_u64 v[0:1], s[42:43], 0, v[0:1]
	v_lshl_add_u64 v[0:1], v[0:1], 0, s[96:97]
	s_mov_b32 s57, s97
	v_lshl_add_u64 v[4:5], v[0:1], 0, v[142:143]
	v_lshl_add_u64 v[6:7], v[130:131], 0, s[56:57]
	global_load_dwordx4 v[0:3], v[6:7], off
	v_lshl_add_u64 v[8:9], v[4:5], 0, s[48:49]
	global_load_dwordx2 v[26:27], v[8:9], off
	s_nop 0
	global_load_dwordx4 v[4:7], v[6:7], off offset:64
	s_nop 0
	global_load_dwordx2 v[24:25], v[8:9], off offset:32
	s_mov_b64 s[56:57], 0
	s_mov_b32 s53, 16
	v_mov_b32_e32 v29, v181
	v_lshl_add_u64 v[32:33], v[10:11], 0, s[48:49]
	s_movk_i32 s58, 0x10
	v_or_b32_e32 v84, s58, v86
	v_lshl_add_u64 v[12:13], s[54:55], 0, v[84:85]
	v_mov_b64_e32 v[14:15], s[88:89]
	v_mad_u64_u32 v[14:15], s[58:59], v12, s65, v[14:15]
	v_mov_b32_e32 v18, v15
	v_mad_u64_u32 v[18:19], s[58:59], v13, s65, v[18:19]
	v_mov_b32_e32 v15, v18
	v_lshl_add_u64 v[14:15], v[14:15], 0, s[96:97]
	v_lshl_add_u64 v[14:15], v[14:15], 0, v[142:143]
	v_lshl_add_u64 v[14:15], v[14:15], 0, s[48:49]
	v_lshl_add_u64 v[20:21], v[14:15], 0, s[50:51]
	v_add_co_u32_e32 v14, vcc, s73, v14
	v_lshlrev_b64 v[12:13], 11, v[12:13]
	s_nop 0
	v_addc_co_u32_e32 v15, vcc, 0, v15, vcc
	global_load_dwordx2 v[40:41], v[14:15], off offset:2560
	v_lshl_add_u64 v[14:15], v[32:33], 0, v[12:13]
	global_load_dwordx2 v[42:43], v[14:15], off
	s_nop 0
	global_load_dwordx2 v[44:45], v[20:21], off offset:32
	s_nop 0
	global_load_dwordx2 v[46:47], v[14:15], off offset:32
	s_movk_i32 s58, 0x20
	v_or_b32_e32 v84, s58, v86
	v_lshl_add_u64 v[12:13], s[54:55], 0, v[84:85]
	v_mov_b64_e32 v[14:15], s[88:89]
	v_mad_u64_u32 v[14:15], s[58:59], v12, s65, v[14:15]
	v_mov_b32_e32 v18, v15
	v_mad_u64_u32 v[18:19], s[58:59], v13, s65, v[18:19]
	v_mov_b32_e32 v15, v18
	v_lshl_add_u64 v[14:15], v[14:15], 0, s[96:97]
	v_lshl_add_u64 v[14:15], v[14:15], 0, v[142:143]
	v_lshl_add_u64 v[14:15], v[14:15], 0, s[48:49]
	v_lshl_add_u64 v[20:21], v[14:15], 0, s[50:51]
	v_add_co_u32_e32 v14, vcc, s73, v14
	v_lshlrev_b64 v[12:13], 11, v[12:13]
	s_nop 0
	v_addc_co_u32_e32 v15, vcc, 0, v15, vcc
	global_load_dwordx2 v[48:49], v[14:15], off offset:2560
	v_lshl_add_u64 v[14:15], v[32:33], 0, v[12:13]
	global_load_dwordx2 v[50:51], v[14:15], off
	s_nop 0
	global_load_dwordx2 v[52:53], v[20:21], off offset:32
	s_nop 0
	global_load_dwordx2 v[54:55], v[14:15], off offset:32
	s_movk_i32 s58, 0x30
	v_or_b32_e32 v84, s58, v86
	v_lshl_add_u64 v[12:13], s[54:55], 0, v[84:85]
	v_mov_b64_e32 v[14:15], s[88:89]
	v_mad_u64_u32 v[14:15], s[58:59], v12, s65, v[14:15]
	v_mov_b32_e32 v18, v15
	v_mad_u64_u32 v[18:19], s[58:59], v13, s65, v[18:19]
	v_mov_b32_e32 v15, v18
	v_lshl_add_u64 v[14:15], v[14:15], 0, s[96:97]
	v_lshl_add_u64 v[14:15], v[14:15], 0, v[142:143]
	v_lshl_add_u64 v[14:15], v[14:15], 0, s[48:49]
	v_lshl_add_u64 v[20:21], v[14:15], 0, s[50:51]
	v_add_co_u32_e32 v14, vcc, s73, v14
	v_lshlrev_b64 v[12:13], 11, v[12:13]
	s_nop 0
	v_addc_co_u32_e32 v15, vcc, 0, v15, vcc
	global_load_dwordx2 v[56:57], v[14:15], off offset:2560
	v_lshl_add_u64 v[14:15], v[32:33], 0, v[12:13]
	global_load_dwordx2 v[58:59], v[14:15], off
	s_nop 0
	global_load_dwordx2 v[60:61], v[20:21], off offset:32
	s_nop 0
	global_load_dwordx2 v[62:63], v[14:15], off offset:32
	s_movk_i32 s58, 0x40
	v_or_b32_e32 v84, s58, v86
	v_lshl_add_u64 v[12:13], s[54:55], 0, v[84:85]
	v_mov_b64_e32 v[14:15], s[88:89]
	v_mad_u64_u32 v[14:15], s[58:59], v12, s65, v[14:15]
	v_mov_b32_e32 v18, v15
	v_mad_u64_u32 v[18:19], s[58:59], v13, s65, v[18:19]
	v_mov_b32_e32 v15, v18
	v_lshl_add_u64 v[14:15], v[14:15], 0, s[96:97]
	v_lshl_add_u64 v[14:15], v[14:15], 0, v[142:143]
	v_lshl_add_u64 v[14:15], v[14:15], 0, s[48:49]
	v_lshl_add_u64 v[20:21], v[14:15], 0, s[50:51]
	v_add_co_u32_e32 v14, vcc, s73, v14
	v_lshlrev_b64 v[12:13], 11, v[12:13]
	s_nop 0
	v_addc_co_u32_e32 v15, vcc, 0, v15, vcc
	global_load_dwordx2 v[64:65], v[14:15], off offset:2560
	v_lshl_add_u64 v[14:15], v[32:33], 0, v[12:13]
	global_load_dwordx2 v[66:67], v[14:15], off
	s_nop 0
	global_load_dwordx2 v[68:69], v[20:21], off offset:32
	s_nop 0
	global_load_dwordx2 v[70:71], v[14:15], off offset:32
	s_movk_i32 s58, 0x50
	v_or_b32_e32 v84, s58, v86
	v_lshl_add_u64 v[12:13], s[54:55], 0, v[84:85]
	v_mov_b64_e32 v[14:15], s[88:89]
	v_mad_u64_u32 v[14:15], s[58:59], v12, s65, v[14:15]
	v_mov_b32_e32 v18, v15
	v_mad_u64_u32 v[18:19], s[58:59], v13, s65, v[18:19]
	v_mov_b32_e32 v15, v18
	v_lshl_add_u64 v[14:15], v[14:15], 0, s[96:97]
	v_lshl_add_u64 v[14:15], v[14:15], 0, v[142:143]
	v_lshl_add_u64 v[14:15], v[14:15], 0, s[48:49]
	v_lshl_add_u64 v[20:21], v[14:15], 0, s[50:51]
	v_add_co_u32_e32 v14, vcc, s73, v14
	v_lshlrev_b64 v[12:13], 11, v[12:13]
	s_nop 0
	v_addc_co_u32_e32 v15, vcc, 0, v15, vcc
	global_load_dwordx2 v[72:73], v[14:15], off offset:2560
	v_lshl_add_u64 v[14:15], v[32:33], 0, v[12:13]
	global_load_dwordx2 v[74:75], v[14:15], off
	s_nop 0
	global_load_dwordx2 v[76:77], v[20:21], off offset:32
	s_nop 0
	global_load_dwordx2 v[78:79], v[14:15], off offset:32
	s_movk_i32 s58, 0x60
	v_or_b32_e32 v84, s58, v86
	v_lshl_add_u64 v[12:13], s[54:55], 0, v[84:85]
	v_mov_b64_e32 v[14:15], s[88:89]
	v_mad_u64_u32 v[14:15], s[58:59], v12, s65, v[14:15]
	v_mov_b32_e32 v18, v15
	v_mad_u64_u32 v[18:19], s[58:59], v13, s65, v[18:19]
	v_mov_b32_e32 v15, v18
	v_lshl_add_u64 v[14:15], v[14:15], 0, s[96:97]
	v_lshl_add_u64 v[14:15], v[14:15], 0, v[142:143]
	v_lshl_add_u64 v[14:15], v[14:15], 0, s[48:49]
	v_lshl_add_u64 v[20:21], v[14:15], 0, s[50:51]
	v_add_co_u32_e32 v14, vcc, s73, v14
	v_lshlrev_b64 v[12:13], 11, v[12:13]
	s_nop 0
	v_addc_co_u32_e32 v15, vcc, 0, v15, vcc
	global_load_dwordx2 v[200:201], v[14:15], off offset:2560
	v_lshl_add_u64 v[14:15], v[32:33], 0, v[12:13]
	global_load_dwordx2 v[202:203], v[14:15], off
	s_nop 0
	global_load_dwordx2 v[204:205], v[20:21], off offset:32
	s_nop 0
	global_load_dwordx2 v[206:207], v[14:15], off offset:32
	s_movk_i32 s58, 0x70
	v_or_b32_e32 v84, s58, v86
	v_lshl_add_u64 v[12:13], s[54:55], 0, v[84:85]
	v_mov_b64_e32 v[14:15], s[88:89]
	v_mad_u64_u32 v[14:15], s[58:59], v12, s65, v[14:15]
	v_mov_b32_e32 v18, v15
	v_mad_u64_u32 v[18:19], s[58:59], v13, s65, v[18:19]
	v_mov_b32_e32 v15, v18
	v_lshl_add_u64 v[14:15], v[14:15], 0, s[96:97]
	v_lshl_add_u64 v[14:15], v[14:15], 0, v[142:143]
	v_lshl_add_u64 v[14:15], v[14:15], 0, s[48:49]
	v_lshl_add_u64 v[20:21], v[14:15], 0, s[50:51]
	v_add_co_u32_e32 v14, vcc, s73, v14
	v_lshlrev_b64 v[12:13], 11, v[12:13]
	s_nop 0
	v_addc_co_u32_e32 v15, vcc, 0, v15, vcc
	global_load_dwordx2 v[208:209], v[14:15], off offset:2560
	v_lshl_add_u64 v[14:15], v[32:33], 0, v[12:13]
	global_load_dwordx2 v[210:211], v[14:15], off
	s_nop 0
	global_load_dwordx2 v[212:213], v[20:21], off offset:32
	s_nop 0
	global_load_dwordx2 v[214:215], v[14:15], off offset:32
	s_barrier
	s_waitcnt vmcnt(31)
	v_mov_b32_e32 v8, v1
	v_mov_b32_e32 v9, v3
	v_mov_b32_e32 v1, v2
	s_waitcnt vmcnt(29)
	v_mov_b32_e32 v2, v5
	v_mov_b32_e32 v3, v7
	v_mov_b32_e32 v5, v6
	v_lshl_add_u64 v[6:7], v[10:11], 0, s[48:49]
	v_lshl_add_u64 v[10:11], v[134:135], 0, v[144:145]
	s_waitcnt vmcnt(28)
	v_add_u32_e32 v28, -16, v29
	ds_read_b128 v[30:33], v28
	ds_read_b128 v[34:37], v29
	s_mov_b32 s58, 0x800000
	s_waitcnt lgkmcnt(1)
	v_mov_b32_e32 v38, v31
	v_mov_b32_e32 v39, v32
	v_mov_b32_e32 v31, v33
	v_pk_add_f32 v[30:31], v[38:39], v[30:31]
	s_waitcnt lgkmcnt(0)
	v_mov_b32_e32 v32, v36
	v_mov_b32_e32 v33, v34
	v_mov_b32_e32 v34, v37
	v_pk_add_f32 v[32:33], v[32:33], v[34:35]
	v_add_f32_e32 v28, v30, v31
	v_add_f32_e32 v28, v28, v33
	v_add_f32_e32 v28, v32, v28
	v_fmamk_f32 v28, v28, 0x3b800000, v195
	v_cmp_gt_f32_e32 vcc, s58, v28
	v_mul_f32_e32 v30, 0x4b800000, v28
	v_lshlrev_b32_e32 v33, 16, v27
	v_cndmask_b32_e32 v28, v28, v30, vcc
	v_rsq_f32_e32 v28, v28
	v_lshlrev_b32_e32 v32, 16, v26
	v_and_b32_e32 v27, 0xffff0000, v27
	v_and_b32_e32 v26, 0xffff0000, v26
	v_mul_f32_e32 v30, 0x45800000, v28
	v_cndmask_b32_e32 v28, v28, v30, vcc
	v_pk_mul_f32 v[32:33], v[28:29], v[32:33] op_sel_hi:[0,1]
	v_pk_mul_f32 v[32:33], v[0:1], v[32:33]
	v_lshlrev_b32_e32 v35, 16, v23
	v_lshlrev_b32_e32 v34, 16, v22
	v_pk_mul_f32 v[26:27], v[28:29], v[26:27] op_sel_hi:[0,1]
	v_pk_mul_f32 v[32:33], v[32:33], v[34:35]
	v_pk_mul_f32 v[26:27], v[8:9], v[26:27]
	v_and_b32_e32 v23, 0xffff0000, v23
	v_and_b32_e32 v22, 0xffff0000, v22
	v_pk_mul_f32 v[22:23], v[26:27], v[22:23]
	v_and_b32_sdwa v27, v32, v198 dst_sel:DWORD dst_unused:UNUSED_PAD src0_sel:WORD_1 src1_sel:DWORD
	v_and_b32_sdwa v26, v33, v198 dst_sel:DWORD dst_unused:UNUSED_PAD src0_sel:WORD_1 src1_sel:DWORD
	v_add3_u32 v27, v32, v27, s71
	v_and_b32_sdwa v32, v23, v198 dst_sel:DWORD dst_unused:UNUSED_PAD src0_sel:WORD_1 src1_sel:DWORD
	v_add3_u32 v26, v33, v26, s71
	v_and_b32_sdwa v33, v22, v198 dst_sel:DWORD dst_unused:UNUSED_PAD src0_sel:WORD_1 src1_sel:DWORD
	v_add3_u32 v23, v23, v32, s71
	v_lshl_add_u64 v[30:31], v[10:11], 0, s[56:57]
	v_add3_u32 v22, v22, v33, s71
	v_and_b32_e32 v23, 0xffff0000, v23
	v_and_b32_e32 v22, 0xffff0000, v22
	v_or_b32_sdwa v23, v23, v26 dst_sel:DWORD dst_unused:UNUSED_PAD src0_sel:DWORD src1_sel:WORD_1
	v_add_co_u32_e32 v26, vcc, s72, v30
	v_or_b32_sdwa v22, v22, v27 dst_sel:DWORD dst_unused:UNUSED_PAD src0_sel:DWORD src1_sel:WORD_1
	s_nop 0
	v_addc_co_u32_e32 v27, vcc, 0, v31, vcc
	global_store_dwordx2 v[26:27], v[22:23], off offset:3072
	v_lshlrev_b32_e32 v23, 16, v25
	v_lshlrev_b32_e32 v22, 16, v24
	v_pk_mul_f32 v[22:23], v[28:29], v[22:23] op_sel_hi:[0,1]
	v_and_b32_e32 v25, 0xffff0000, v25
	v_and_b32_e32 v24, 0xffff0000, v24
	v_pk_mul_f32 v[22:23], v[4:5], v[22:23]
	v_lshlrev_b32_e32 v31, 16, v17
	v_lshlrev_b32_e32 v30, 16, v16
	v_pk_mul_f32 v[24:25], v[28:29], v[24:25] op_sel_hi:[0,1]
	v_pk_mul_f32 v[22:23], v[22:23], v[30:31]
	v_pk_mul_f32 v[24:25], v[2:3], v[24:25]
	v_and_b32_e32 v17, 0xffff0000, v17
	v_and_b32_e32 v16, 0xffff0000, v16
	v_pk_mul_f32 v[16:17], v[24:25], v[16:17]
	v_and_b32_sdwa v24, v23, v198 dst_sel:DWORD dst_unused:UNUSED_PAD src0_sel:WORD_1 src1_sel:DWORD
	v_and_b32_sdwa v25, v22, v198 dst_sel:DWORD dst_unused:UNUSED_PAD src0_sel:WORD_1 src1_sel:DWORD
	v_add3_u32 v22, v22, v25, s71
	v_add3_u32 v23, v23, v24, s71
	v_and_b32_sdwa v24, v17, v198 dst_sel:DWORD dst_unused:UNUSED_PAD src0_sel:WORD_1 src1_sel:DWORD
	v_and_b32_sdwa v25, v16, v198 dst_sel:DWORD dst_unused:UNUSED_PAD src0_sel:WORD_1 src1_sel:DWORD
	v_add3_u32 v17, v17, v24, s71
	v_add3_u32 v16, v16, v25, s71
	v_and_b32_e32 v17, 0xffff0000, v17
	v_and_b32_e32 v16, 0xffff0000, v16
	s_add_u32 s56, s56, 0x8000
	v_or_b32_sdwa v17, v17, v23 dst_sel:DWORD dst_unused:UNUSED_PAD src0_sel:DWORD src1_sel:WORD_1
	v_or_b32_sdwa v16, v16, v22 dst_sel:DWORD dst_unused:UNUSED_PAD src0_sel:DWORD src1_sel:WORD_1
	s_addc_u32 s57, s57, 0
	global_store_dwordx2 v[26:27], v[16:17], off offset:3104
	v_add_u32_e32 v29, 0x200, v29
	s_waitcnt vmcnt(26)
	v_add_u32_e32 v28, -16, v29
	ds_read_b128 v[30:33], v28
	ds_read_b128 v[34:37], v29
	s_mov_b32 s58, 0x800000
	s_waitcnt lgkmcnt(1)
	v_mov_b32_e32 v38, v31
	v_mov_b32_e32 v39, v32
	v_mov_b32_e32 v31, v33
	v_pk_add_f32 v[30:31], v[38:39], v[30:31]
	s_waitcnt lgkmcnt(0)
	v_mov_b32_e32 v32, v36
	v_mov_b32_e32 v33, v34
	v_mov_b32_e32 v34, v37
	v_pk_add_f32 v[32:33], v[32:33], v[34:35]
	v_add_f32_e32 v28, v30, v31
	v_add_f32_e32 v28, v28, v33
	v_add_f32_e32 v28, v32, v28
	v_fmamk_f32 v28, v28, 0x3b800000, v195
	v_cmp_gt_f32_e32 vcc, s58, v28
	v_mul_f32_e32 v30, 0x4b800000, v28
	v_lshlrev_b32_e32 v33, 16, v43
	v_cndmask_b32_e32 v28, v28, v30, vcc
	v_rsq_f32_e32 v28, v28
	v_lshlrev_b32_e32 v32, 16, v42
	v_and_b32_e32 v43, 0xffff0000, v43
	v_and_b32_e32 v42, 0xffff0000, v42
	v_mul_f32_e32 v30, 0x45800000, v28
	v_cndmask_b32_e32 v28, v28, v30, vcc
	v_pk_mul_f32 v[32:33], v[28:29], v[32:33] op_sel_hi:[0,1]
	v_pk_mul_f32 v[32:33], v[0:1], v[32:33]
	v_lshlrev_b32_e32 v35, 16, v41
	v_lshlrev_b32_e32 v34, 16, v40
	v_pk_mul_f32 v[42:43], v[28:29], v[42:43] op_sel_hi:[0,1]
	v_pk_mul_f32 v[32:33], v[32:33], v[34:35]
	v_pk_mul_f32 v[42:43], v[8:9], v[42:43]
	v_and_b32_e32 v41, 0xffff0000, v41
	v_and_b32_e32 v40, 0xffff0000, v40
	v_pk_mul_f32 v[40:41], v[42:43], v[40:41]
	v_and_b32_sdwa v43, v32, v198 dst_sel:DWORD dst_unused:UNUSED_PAD src0_sel:WORD_1 src1_sel:DWORD
	v_and_b32_sdwa v42, v33, v198 dst_sel:DWORD dst_unused:UNUSED_PAD src0_sel:WORD_1 src1_sel:DWORD
	v_add3_u32 v43, v32, v43, s71
	v_and_b32_sdwa v32, v41, v198 dst_sel:DWORD dst_unused:UNUSED_PAD src0_sel:WORD_1 src1_sel:DWORD
	v_add3_u32 v42, v33, v42, s71
	v_and_b32_sdwa v33, v40, v198 dst_sel:DWORD dst_unused:UNUSED_PAD src0_sel:WORD_1 src1_sel:DWORD
	v_add3_u32 v41, v41, v32, s71
	v_lshl_add_u64 v[30:31], v[10:11], 0, s[56:57]
	v_add3_u32 v40, v40, v33, s71
	v_and_b32_e32 v41, 0xffff0000, v41
	v_and_b32_e32 v40, 0xffff0000, v40
	v_or_b32_sdwa v41, v41, v42 dst_sel:DWORD dst_unused:UNUSED_PAD src0_sel:DWORD src1_sel:WORD_1
	v_add_co_u32_e32 v42, vcc, s72, v30
	v_or_b32_sdwa v40, v40, v43 dst_sel:DWORD dst_unused:UNUSED_PAD src0_sel:DWORD src1_sel:WORD_1
	s_nop 0
	v_addc_co_u32_e32 v43, vcc, 0, v31, vcc
	global_store_dwordx2 v[42:43], v[40:41], off offset:3072
	v_lshlrev_b32_e32 v41, 16, v47
	v_lshlrev_b32_e32 v40, 16, v46
	v_pk_mul_f32 v[40:41], v[28:29], v[40:41] op_sel_hi:[0,1]
	v_and_b32_e32 v47, 0xffff0000, v47
	v_and_b32_e32 v46, 0xffff0000, v46
	v_pk_mul_f32 v[40:41], v[4:5], v[40:41]
	v_lshlrev_b32_e32 v31, 16, v45
	v_lshlrev_b32_e32 v30, 16, v44
	v_pk_mul_f32 v[46:47], v[28:29], v[46:47] op_sel_hi:[0,1]
	v_pk_mul_f32 v[40:41], v[40:41], v[30:31]
	v_pk_mul_f32 v[46:47], v[2:3], v[46:47]
	v_and_b32_e32 v45, 0xffff0000, v45
	v_and_b32_e32 v44, 0xffff0000, v44
	v_pk_mul_f32 v[44:45], v[46:47], v[44:45]
	v_and_b32_sdwa v46, v41, v198 dst_sel:DWORD dst_unused:UNUSED_PAD src0_sel:WORD_1 src1_sel:DWORD
	v_and_b32_sdwa v47, v40, v198 dst_sel:DWORD dst_unused:UNUSED_PAD src0_sel:WORD_1 src1_sel:DWORD
	v_add3_u32 v40, v40, v47, s71
	v_add3_u32 v41, v41, v46, s71
	v_and_b32_sdwa v46, v45, v198 dst_sel:DWORD dst_unused:UNUSED_PAD src0_sel:WORD_1 src1_sel:DWORD
	v_and_b32_sdwa v47, v44, v198 dst_sel:DWORD dst_unused:UNUSED_PAD src0_sel:WORD_1 src1_sel:DWORD
	v_add3_u32 v45, v45, v46, s71
	v_add3_u32 v44, v44, v47, s71
	v_and_b32_e32 v45, 0xffff0000, v45
	v_and_b32_e32 v44, 0xffff0000, v44
	s_add_u32 s56, s56, 0x8000
	v_or_b32_sdwa v45, v45, v41 dst_sel:DWORD dst_unused:UNUSED_PAD src0_sel:DWORD src1_sel:WORD_1
	v_or_b32_sdwa v44, v44, v40 dst_sel:DWORD dst_unused:UNUSED_PAD src0_sel:DWORD src1_sel:WORD_1
	s_addc_u32 s57, s57, 0
	global_store_dwordx2 v[42:43], v[44:45], off offset:3104
	v_add_u32_e32 v29, 0x200, v29
	s_waitcnt vmcnt(24)
	v_add_u32_e32 v28, -16, v29
	ds_read_b128 v[30:33], v28
	ds_read_b128 v[34:37], v29
	s_mov_b32 s58, 0x800000
	s_waitcnt lgkmcnt(1)
	v_mov_b32_e32 v38, v31
	v_mov_b32_e32 v39, v32
	v_mov_b32_e32 v31, v33
	v_pk_add_f32 v[30:31], v[38:39], v[30:31]
	s_waitcnt lgkmcnt(0)
	v_mov_b32_e32 v32, v36
	v_mov_b32_e32 v33, v34
	v_mov_b32_e32 v34, v37
	v_pk_add_f32 v[32:33], v[32:33], v[34:35]
	v_add_f32_e32 v28, v30, v31
	v_add_f32_e32 v28, v28, v33
	v_add_f32_e32 v28, v32, v28
	v_fmamk_f32 v28, v28, 0x3b800000, v195
	v_cmp_gt_f32_e32 vcc, s58, v28
	v_mul_f32_e32 v30, 0x4b800000, v28
	v_lshlrev_b32_e32 v33, 16, v51
	v_cndmask_b32_e32 v28, v28, v30, vcc
	v_rsq_f32_e32 v28, v28
	v_lshlrev_b32_e32 v32, 16, v50
	v_and_b32_e32 v51, 0xffff0000, v51
	v_and_b32_e32 v50, 0xffff0000, v50
	v_mul_f32_e32 v30, 0x45800000, v28
	v_cndmask_b32_e32 v28, v28, v30, vcc
	v_pk_mul_f32 v[32:33], v[28:29], v[32:33] op_sel_hi:[0,1]
	v_pk_mul_f32 v[32:33], v[0:1], v[32:33]
	v_lshlrev_b32_e32 v35, 16, v49
	v_lshlrev_b32_e32 v34, 16, v48
	v_pk_mul_f32 v[50:51], v[28:29], v[50:51] op_sel_hi:[0,1]
	v_pk_mul_f32 v[32:33], v[32:33], v[34:35]
	v_pk_mul_f32 v[50:51], v[8:9], v[50:51]
	v_and_b32_e32 v49, 0xffff0000, v49
	v_and_b32_e32 v48, 0xffff0000, v48
	v_pk_mul_f32 v[48:49], v[50:51], v[48:49]
	v_and_b32_sdwa v51, v32, v198 dst_sel:DWORD dst_unused:UNUSED_PAD src0_sel:WORD_1 src1_sel:DWORD
	v_and_b32_sdwa v50, v33, v198 dst_sel:DWORD dst_unused:UNUSED_PAD src0_sel:WORD_1 src1_sel:DWORD
	v_add3_u32 v51, v32, v51, s71
	v_and_b32_sdwa v32, v49, v198 dst_sel:DWORD dst_unused:UNUSED_PAD src0_sel:WORD_1 src1_sel:DWORD
	v_add3_u32 v50, v33, v50, s71
	v_and_b32_sdwa v33, v48, v198 dst_sel:DWORD dst_unused:UNUSED_PAD src0_sel:WORD_1 src1_sel:DWORD
	v_add3_u32 v49, v49, v32, s71
	v_lshl_add_u64 v[30:31], v[10:11], 0, s[56:57]
	v_add3_u32 v48, v48, v33, s71
	v_and_b32_e32 v49, 0xffff0000, v49
	v_and_b32_e32 v48, 0xffff0000, v48
	v_or_b32_sdwa v49, v49, v50 dst_sel:DWORD dst_unused:UNUSED_PAD src0_sel:DWORD src1_sel:WORD_1
	v_add_co_u32_e32 v50, vcc, s72, v30
	v_or_b32_sdwa v48, v48, v51 dst_sel:DWORD dst_unused:UNUSED_PAD src0_sel:DWORD src1_sel:WORD_1
	s_nop 0
	v_addc_co_u32_e32 v51, vcc, 0, v31, vcc
	global_store_dwordx2 v[50:51], v[48:49], off offset:3072
	v_lshlrev_b32_e32 v49, 16, v55
	v_lshlrev_b32_e32 v48, 16, v54
	v_pk_mul_f32 v[48:49], v[28:29], v[48:49] op_sel_hi:[0,1]
	v_and_b32_e32 v55, 0xffff0000, v55
	v_and_b32_e32 v54, 0xffff0000, v54
	v_pk_mul_f32 v[48:49], v[4:5], v[48:49]
	v_lshlrev_b32_e32 v31, 16, v53
	v_lshlrev_b32_e32 v30, 16, v52
	v_pk_mul_f32 v[54:55], v[28:29], v[54:55] op_sel_hi:[0,1]
	v_pk_mul_f32 v[48:49], v[48:49], v[30:31]
	v_pk_mul_f32 v[54:55], v[2:3], v[54:55]
	v_and_b32_e32 v53, 0xffff0000, v53
	v_and_b32_e32 v52, 0xffff0000, v52
	v_pk_mul_f32 v[52:53], v[54:55], v[52:53]
	v_and_b32_sdwa v54, v49, v198 dst_sel:DWORD dst_unused:UNUSED_PAD src0_sel:WORD_1 src1_sel:DWORD
	v_and_b32_sdwa v55, v48, v198 dst_sel:DWORD dst_unused:UNUSED_PAD src0_sel:WORD_1 src1_sel:DWORD
	v_add3_u32 v48, v48, v55, s71
	v_add3_u32 v49, v49, v54, s71
	v_and_b32_sdwa v54, v53, v198 dst_sel:DWORD dst_unused:UNUSED_PAD src0_sel:WORD_1 src1_sel:DWORD
	v_and_b32_sdwa v55, v52, v198 dst_sel:DWORD dst_unused:UNUSED_PAD src0_sel:WORD_1 src1_sel:DWORD
	v_add3_u32 v53, v53, v54, s71
	v_add3_u32 v52, v52, v55, s71
	v_and_b32_e32 v53, 0xffff0000, v53
	v_and_b32_e32 v52, 0xffff0000, v52
	s_add_u32 s56, s56, 0x8000
	v_or_b32_sdwa v53, v53, v49 dst_sel:DWORD dst_unused:UNUSED_PAD src0_sel:DWORD src1_sel:WORD_1
	v_or_b32_sdwa v52, v52, v48 dst_sel:DWORD dst_unused:UNUSED_PAD src0_sel:DWORD src1_sel:WORD_1
	s_addc_u32 s57, s57, 0
	global_store_dwordx2 v[50:51], v[52:53], off offset:3104
	v_add_u32_e32 v29, 0x200, v29
	s_waitcnt vmcnt(22)
	v_add_u32_e32 v28, -16, v29
	ds_read_b128 v[30:33], v28
	ds_read_b128 v[34:37], v29
	s_mov_b32 s58, 0x800000
	s_waitcnt lgkmcnt(1)
	v_mov_b32_e32 v38, v31
	v_mov_b32_e32 v39, v32
	v_mov_b32_e32 v31, v33
	v_pk_add_f32 v[30:31], v[38:39], v[30:31]
	s_waitcnt lgkmcnt(0)
	v_mov_b32_e32 v32, v36
	v_mov_b32_e32 v33, v34
	v_mov_b32_e32 v34, v37
	v_pk_add_f32 v[32:33], v[32:33], v[34:35]
	v_add_f32_e32 v28, v30, v31
	v_add_f32_e32 v28, v28, v33
	v_add_f32_e32 v28, v32, v28
	v_fmamk_f32 v28, v28, 0x3b800000, v195
	v_cmp_gt_f32_e32 vcc, s58, v28
	v_mul_f32_e32 v30, 0x4b800000, v28
	v_lshlrev_b32_e32 v33, 16, v59
	v_cndmask_b32_e32 v28, v28, v30, vcc
	v_rsq_f32_e32 v28, v28
	v_lshlrev_b32_e32 v32, 16, v58
	v_and_b32_e32 v59, 0xffff0000, v59
	v_and_b32_e32 v58, 0xffff0000, v58
	v_mul_f32_e32 v30, 0x45800000, v28
	v_cndmask_b32_e32 v28, v28, v30, vcc
	v_pk_mul_f32 v[32:33], v[28:29], v[32:33] op_sel_hi:[0,1]
	v_pk_mul_f32 v[32:33], v[0:1], v[32:33]
	v_lshlrev_b32_e32 v35, 16, v57
	v_lshlrev_b32_e32 v34, 16, v56
	v_pk_mul_f32 v[58:59], v[28:29], v[58:59] op_sel_hi:[0,1]
	v_pk_mul_f32 v[32:33], v[32:33], v[34:35]
	v_pk_mul_f32 v[58:59], v[8:9], v[58:59]
	v_and_b32_e32 v57, 0xffff0000, v57
	v_and_b32_e32 v56, 0xffff0000, v56
	v_pk_mul_f32 v[56:57], v[58:59], v[56:57]
	v_and_b32_sdwa v59, v32, v198 dst_sel:DWORD dst_unused:UNUSED_PAD src0_sel:WORD_1 src1_sel:DWORD
	v_and_b32_sdwa v58, v33, v198 dst_sel:DWORD dst_unused:UNUSED_PAD src0_sel:WORD_1 src1_sel:DWORD
	v_add3_u32 v59, v32, v59, s71
	v_and_b32_sdwa v32, v57, v198 dst_sel:DWORD dst_unused:UNUSED_PAD src0_sel:WORD_1 src1_sel:DWORD
	v_add3_u32 v58, v33, v58, s71
	v_and_b32_sdwa v33, v56, v198 dst_sel:DWORD dst_unused:UNUSED_PAD src0_sel:WORD_1 src1_sel:DWORD
	v_add3_u32 v57, v57, v32, s71
	v_lshl_add_u64 v[30:31], v[10:11], 0, s[56:57]
	v_add3_u32 v56, v56, v33, s71
	v_and_b32_e32 v57, 0xffff0000, v57
	v_and_b32_e32 v56, 0xffff0000, v56
	v_or_b32_sdwa v57, v57, v58 dst_sel:DWORD dst_unused:UNUSED_PAD src0_sel:DWORD src1_sel:WORD_1
	v_add_co_u32_e32 v58, vcc, s72, v30
	v_or_b32_sdwa v56, v56, v59 dst_sel:DWORD dst_unused:UNUSED_PAD src0_sel:DWORD src1_sel:WORD_1
	s_nop 0
	v_addc_co_u32_e32 v59, vcc, 0, v31, vcc
	global_store_dwordx2 v[58:59], v[56:57], off offset:3072
	v_lshlrev_b32_e32 v57, 16, v63
	v_lshlrev_b32_e32 v56, 16, v62
	v_pk_mul_f32 v[56:57], v[28:29], v[56:57] op_sel_hi:[0,1]
	v_and_b32_e32 v63, 0xffff0000, v63
	v_and_b32_e32 v62, 0xffff0000, v62
	v_pk_mul_f32 v[56:57], v[4:5], v[56:57]
	v_lshlrev_b32_e32 v31, 16, v61
	v_lshlrev_b32_e32 v30, 16, v60
	v_pk_mul_f32 v[62:63], v[28:29], v[62:63] op_sel_hi:[0,1]
	v_pk_mul_f32 v[56:57], v[56:57], v[30:31]
	v_pk_mul_f32 v[62:63], v[2:3], v[62:63]
	v_and_b32_e32 v61, 0xffff0000, v61
	v_and_b32_e32 v60, 0xffff0000, v60
	v_pk_mul_f32 v[60:61], v[62:63], v[60:61]
	v_and_b32_sdwa v62, v57, v198 dst_sel:DWORD dst_unused:UNUSED_PAD src0_sel:WORD_1 src1_sel:DWORD
	v_and_b32_sdwa v63, v56, v198 dst_sel:DWORD dst_unused:UNUSED_PAD src0_sel:WORD_1 src1_sel:DWORD
	v_add3_u32 v56, v56, v63, s71
	v_add3_u32 v57, v57, v62, s71
	v_and_b32_sdwa v62, v61, v198 dst_sel:DWORD dst_unused:UNUSED_PAD src0_sel:WORD_1 src1_sel:DWORD
	v_and_b32_sdwa v63, v60, v198 dst_sel:DWORD dst_unused:UNUSED_PAD src0_sel:WORD_1 src1_sel:DWORD
	v_add3_u32 v61, v61, v62, s71
	v_add3_u32 v60, v60, v63, s71
	v_and_b32_e32 v61, 0xffff0000, v61
	v_and_b32_e32 v60, 0xffff0000, v60
	s_add_u32 s56, s56, 0x8000
	v_or_b32_sdwa v61, v61, v57 dst_sel:DWORD dst_unused:UNUSED_PAD src0_sel:DWORD src1_sel:WORD_1
	v_or_b32_sdwa v60, v60, v56 dst_sel:DWORD dst_unused:UNUSED_PAD src0_sel:DWORD src1_sel:WORD_1
	s_addc_u32 s57, s57, 0
	global_store_dwordx2 v[58:59], v[60:61], off offset:3104
	v_add_u32_e32 v29, 0x200, v29
	s_waitcnt vmcnt(20)
	v_add_u32_e32 v28, -16, v29
	ds_read_b128 v[30:33], v28
	ds_read_b128 v[34:37], v29
	s_mov_b32 s58, 0x800000
	s_waitcnt lgkmcnt(1)
	v_mov_b32_e32 v38, v31
	v_mov_b32_e32 v39, v32
	v_mov_b32_e32 v31, v33
	v_pk_add_f32 v[30:31], v[38:39], v[30:31]
	s_waitcnt lgkmcnt(0)
	v_mov_b32_e32 v32, v36
	v_mov_b32_e32 v33, v34
	v_mov_b32_e32 v34, v37
	v_pk_add_f32 v[32:33], v[32:33], v[34:35]
	v_add_f32_e32 v28, v30, v31
	v_add_f32_e32 v28, v28, v33
	v_add_f32_e32 v28, v32, v28
	v_fmamk_f32 v28, v28, 0x3b800000, v195
	v_cmp_gt_f32_e32 vcc, s58, v28
	v_mul_f32_e32 v30, 0x4b800000, v28
	v_lshlrev_b32_e32 v33, 16, v67
	v_cndmask_b32_e32 v28, v28, v30, vcc
	v_rsq_f32_e32 v28, v28
	v_lshlrev_b32_e32 v32, 16, v66
	v_and_b32_e32 v67, 0xffff0000, v67
	v_and_b32_e32 v66, 0xffff0000, v66
	v_mul_f32_e32 v30, 0x45800000, v28
	v_cndmask_b32_e32 v28, v28, v30, vcc
	v_pk_mul_f32 v[32:33], v[28:29], v[32:33] op_sel_hi:[0,1]
	v_pk_mul_f32 v[32:33], v[0:1], v[32:33]
	v_lshlrev_b32_e32 v35, 16, v65
	v_lshlrev_b32_e32 v34, 16, v64
	v_pk_mul_f32 v[66:67], v[28:29], v[66:67] op_sel_hi:[0,1]
	v_pk_mul_f32 v[32:33], v[32:33], v[34:35]
	v_pk_mul_f32 v[66:67], v[8:9], v[66:67]
	v_and_b32_e32 v65, 0xffff0000, v65
	v_and_b32_e32 v64, 0xffff0000, v64
	v_pk_mul_f32 v[64:65], v[66:67], v[64:65]
	v_and_b32_sdwa v67, v32, v198 dst_sel:DWORD dst_unused:UNUSED_PAD src0_sel:WORD_1 src1_sel:DWORD
	v_and_b32_sdwa v66, v33, v198 dst_sel:DWORD dst_unused:UNUSED_PAD src0_sel:WORD_1 src1_sel:DWORD
	v_add3_u32 v67, v32, v67, s71
	v_and_b32_sdwa v32, v65, v198 dst_sel:DWORD dst_unused:UNUSED_PAD src0_sel:WORD_1 src1_sel:DWORD
	v_add3_u32 v66, v33, v66, s71
	v_and_b32_sdwa v33, v64, v198 dst_sel:DWORD dst_unused:UNUSED_PAD src0_sel:WORD_1 src1_sel:DWORD
	v_add3_u32 v65, v65, v32, s71
	v_lshl_add_u64 v[30:31], v[10:11], 0, s[56:57]
	v_add3_u32 v64, v64, v33, s71
	v_and_b32_e32 v65, 0xffff0000, v65
	v_and_b32_e32 v64, 0xffff0000, v64
	v_or_b32_sdwa v65, v65, v66 dst_sel:DWORD dst_unused:UNUSED_PAD src0_sel:DWORD src1_sel:WORD_1
	v_add_co_u32_e32 v66, vcc, s72, v30
	v_or_b32_sdwa v64, v64, v67 dst_sel:DWORD dst_unused:UNUSED_PAD src0_sel:DWORD src1_sel:WORD_1
	s_nop 0
	v_addc_co_u32_e32 v67, vcc, 0, v31, vcc
	global_store_dwordx2 v[66:67], v[64:65], off offset:3072
	v_lshlrev_b32_e32 v65, 16, v71
	v_lshlrev_b32_e32 v64, 16, v70
	v_pk_mul_f32 v[64:65], v[28:29], v[64:65] op_sel_hi:[0,1]
	v_and_b32_e32 v71, 0xffff0000, v71
	v_and_b32_e32 v70, 0xffff0000, v70
	v_pk_mul_f32 v[64:65], v[4:5], v[64:65]
	v_lshlrev_b32_e32 v31, 16, v69
	v_lshlrev_b32_e32 v30, 16, v68
	v_pk_mul_f32 v[70:71], v[28:29], v[70:71] op_sel_hi:[0,1]
	v_pk_mul_f32 v[64:65], v[64:65], v[30:31]
	v_pk_mul_f32 v[70:71], v[2:3], v[70:71]
	v_and_b32_e32 v69, 0xffff0000, v69
	v_and_b32_e32 v68, 0xffff0000, v68
	v_pk_mul_f32 v[68:69], v[70:71], v[68:69]
	v_and_b32_sdwa v70, v65, v198 dst_sel:DWORD dst_unused:UNUSED_PAD src0_sel:WORD_1 src1_sel:DWORD
	v_and_b32_sdwa v71, v64, v198 dst_sel:DWORD dst_unused:UNUSED_PAD src0_sel:WORD_1 src1_sel:DWORD
	v_add3_u32 v64, v64, v71, s71
	v_add3_u32 v65, v65, v70, s71
	v_and_b32_sdwa v70, v69, v198 dst_sel:DWORD dst_unused:UNUSED_PAD src0_sel:WORD_1 src1_sel:DWORD
	v_and_b32_sdwa v71, v68, v198 dst_sel:DWORD dst_unused:UNUSED_PAD src0_sel:WORD_1 src1_sel:DWORD
	v_add3_u32 v69, v69, v70, s71
	v_add3_u32 v68, v68, v71, s71
	v_and_b32_e32 v69, 0xffff0000, v69
	v_and_b32_e32 v68, 0xffff0000, v68
	s_add_u32 s56, s56, 0x8000
	v_or_b32_sdwa v69, v69, v65 dst_sel:DWORD dst_unused:UNUSED_PAD src0_sel:DWORD src1_sel:WORD_1
	v_or_b32_sdwa v68, v68, v64 dst_sel:DWORD dst_unused:UNUSED_PAD src0_sel:DWORD src1_sel:WORD_1
	s_addc_u32 s57, s57, 0
	global_store_dwordx2 v[66:67], v[68:69], off offset:3104
	v_add_u32_e32 v29, 0x200, v29
	s_waitcnt vmcnt(18)
	v_add_u32_e32 v28, -16, v29
	ds_read_b128 v[30:33], v28
	ds_read_b128 v[34:37], v29
	s_mov_b32 s58, 0x800000
	s_waitcnt lgkmcnt(1)
	v_mov_b32_e32 v38, v31
	v_mov_b32_e32 v39, v32
	v_mov_b32_e32 v31, v33
	v_pk_add_f32 v[30:31], v[38:39], v[30:31]
	s_waitcnt lgkmcnt(0)
	v_mov_b32_e32 v32, v36
	v_mov_b32_e32 v33, v34
	v_mov_b32_e32 v34, v37
	v_pk_add_f32 v[32:33], v[32:33], v[34:35]
	v_add_f32_e32 v28, v30, v31
	v_add_f32_e32 v28, v28, v33
	v_add_f32_e32 v28, v32, v28
	v_fmamk_f32 v28, v28, 0x3b800000, v195
	v_cmp_gt_f32_e32 vcc, s58, v28
	v_mul_f32_e32 v30, 0x4b800000, v28
	v_lshlrev_b32_e32 v33, 16, v75
	v_cndmask_b32_e32 v28, v28, v30, vcc
	v_rsq_f32_e32 v28, v28
	v_lshlrev_b32_e32 v32, 16, v74
	v_and_b32_e32 v75, 0xffff0000, v75
	v_and_b32_e32 v74, 0xffff0000, v74
	v_mul_f32_e32 v30, 0x45800000, v28
	v_cndmask_b32_e32 v28, v28, v30, vcc
	v_pk_mul_f32 v[32:33], v[28:29], v[32:33] op_sel_hi:[0,1]
	v_pk_mul_f32 v[32:33], v[0:1], v[32:33]
	v_lshlrev_b32_e32 v35, 16, v73
	v_lshlrev_b32_e32 v34, 16, v72
	v_pk_mul_f32 v[74:75], v[28:29], v[74:75] op_sel_hi:[0,1]
	v_pk_mul_f32 v[32:33], v[32:33], v[34:35]
	v_pk_mul_f32 v[74:75], v[8:9], v[74:75]
	v_and_b32_e32 v73, 0xffff0000, v73
	v_and_b32_e32 v72, 0xffff0000, v72
	v_pk_mul_f32 v[72:73], v[74:75], v[72:73]
	v_and_b32_sdwa v75, v32, v198 dst_sel:DWORD dst_unused:UNUSED_PAD src0_sel:WORD_1 src1_sel:DWORD
	v_and_b32_sdwa v74, v33, v198 dst_sel:DWORD dst_unused:UNUSED_PAD src0_sel:WORD_1 src1_sel:DWORD
	v_add3_u32 v75, v32, v75, s71
	v_and_b32_sdwa v32, v73, v198 dst_sel:DWORD dst_unused:UNUSED_PAD src0_sel:WORD_1 src1_sel:DWORD
	v_add3_u32 v74, v33, v74, s71
	v_and_b32_sdwa v33, v72, v198 dst_sel:DWORD dst_unused:UNUSED_PAD src0_sel:WORD_1 src1_sel:DWORD
	v_add3_u32 v73, v73, v32, s71
	v_lshl_add_u64 v[30:31], v[10:11], 0, s[56:57]
	v_add3_u32 v72, v72, v33, s71
	v_and_b32_e32 v73, 0xffff0000, v73
	v_and_b32_e32 v72, 0xffff0000, v72
	v_or_b32_sdwa v73, v73, v74 dst_sel:DWORD dst_unused:UNUSED_PAD src0_sel:DWORD src1_sel:WORD_1
	v_add_co_u32_e32 v74, vcc, s72, v30
	v_or_b32_sdwa v72, v72, v75 dst_sel:DWORD dst_unused:UNUSED_PAD src0_sel:DWORD src1_sel:WORD_1
	s_nop 0
	v_addc_co_u32_e32 v75, vcc, 0, v31, vcc
	global_store_dwordx2 v[74:75], v[72:73], off offset:3072
	v_lshlrev_b32_e32 v73, 16, v79
	v_lshlrev_b32_e32 v72, 16, v78
	v_pk_mul_f32 v[72:73], v[28:29], v[72:73] op_sel_hi:[0,1]
	v_and_b32_e32 v79, 0xffff0000, v79
	v_and_b32_e32 v78, 0xffff0000, v78
	v_pk_mul_f32 v[72:73], v[4:5], v[72:73]
	v_lshlrev_b32_e32 v31, 16, v77
	v_lshlrev_b32_e32 v30, 16, v76
	v_pk_mul_f32 v[78:79], v[28:29], v[78:79] op_sel_hi:[0,1]
	v_pk_mul_f32 v[72:73], v[72:73], v[30:31]
	v_pk_mul_f32 v[78:79], v[2:3], v[78:79]
	v_and_b32_e32 v77, 0xffff0000, v77
	v_and_b32_e32 v76, 0xffff0000, v76
	v_pk_mul_f32 v[76:77], v[78:79], v[76:77]
	v_and_b32_sdwa v78, v73, v198 dst_sel:DWORD dst_unused:UNUSED_PAD src0_sel:WORD_1 src1_sel:DWORD
	v_and_b32_sdwa v79, v72, v198 dst_sel:DWORD dst_unused:UNUSED_PAD src0_sel:WORD_1 src1_sel:DWORD
	v_add3_u32 v72, v72, v79, s71
	v_add3_u32 v73, v73, v78, s71
	v_and_b32_sdwa v78, v77, v198 dst_sel:DWORD dst_unused:UNUSED_PAD src0_sel:WORD_1 src1_sel:DWORD
	v_and_b32_sdwa v79, v76, v198 dst_sel:DWORD dst_unused:UNUSED_PAD src0_sel:WORD_1 src1_sel:DWORD
	v_add3_u32 v77, v77, v78, s71
	v_add3_u32 v76, v76, v79, s71
	v_and_b32_e32 v77, 0xffff0000, v77
	v_and_b32_e32 v76, 0xffff0000, v76
	s_add_u32 s56, s56, 0x8000
	v_or_b32_sdwa v77, v77, v73 dst_sel:DWORD dst_unused:UNUSED_PAD src0_sel:DWORD src1_sel:WORD_1
	v_or_b32_sdwa v76, v76, v72 dst_sel:DWORD dst_unused:UNUSED_PAD src0_sel:DWORD src1_sel:WORD_1
	s_addc_u32 s57, s57, 0
	global_store_dwordx2 v[74:75], v[76:77], off offset:3104
	v_add_u32_e32 v29, 0x200, v29
	s_waitcnt vmcnt(16)
	v_add_u32_e32 v28, -16, v29
	ds_read_b128 v[30:33], v28
	ds_read_b128 v[34:37], v29
	s_mov_b32 s58, 0x800000
	s_waitcnt lgkmcnt(1)
	v_mov_b32_e32 v38, v31
	v_mov_b32_e32 v39, v32
	v_mov_b32_e32 v31, v33
	v_pk_add_f32 v[30:31], v[38:39], v[30:31]
	s_waitcnt lgkmcnt(0)
	v_mov_b32_e32 v32, v36
	v_mov_b32_e32 v33, v34
	v_mov_b32_e32 v34, v37
	v_pk_add_f32 v[32:33], v[32:33], v[34:35]
	v_add_f32_e32 v28, v30, v31
	v_add_f32_e32 v28, v28, v33
	v_add_f32_e32 v28, v32, v28
	v_fmamk_f32 v28, v28, 0x3b800000, v195
	v_cmp_gt_f32_e32 vcc, s58, v28
	v_mul_f32_e32 v30, 0x4b800000, v28
	v_lshlrev_b32_e32 v33, 16, v203
	v_cndmask_b32_e32 v28, v28, v30, vcc
	v_rsq_f32_e32 v28, v28
	v_lshlrev_b32_e32 v32, 16, v202
	v_and_b32_e32 v203, 0xffff0000, v203
	v_and_b32_e32 v202, 0xffff0000, v202
	v_mul_f32_e32 v30, 0x45800000, v28
	v_cndmask_b32_e32 v28, v28, v30, vcc
	v_pk_mul_f32 v[32:33], v[28:29], v[32:33] op_sel_hi:[0,1]
	v_pk_mul_f32 v[32:33], v[0:1], v[32:33]
	v_lshlrev_b32_e32 v35, 16, v201
	v_lshlrev_b32_e32 v34, 16, v200
	v_pk_mul_f32 v[202:203], v[28:29], v[202:203] op_sel_hi:[0,1]
	v_pk_mul_f32 v[32:33], v[32:33], v[34:35]
	v_pk_mul_f32 v[202:203], v[8:9], v[202:203]
	v_and_b32_e32 v201, 0xffff0000, v201
	v_and_b32_e32 v200, 0xffff0000, v200
	v_pk_mul_f32 v[200:201], v[202:203], v[200:201]
	v_and_b32_sdwa v203, v32, v198 dst_sel:DWORD dst_unused:UNUSED_PAD src0_sel:WORD_1 src1_sel:DWORD
	v_and_b32_sdwa v202, v33, v198 dst_sel:DWORD dst_unused:UNUSED_PAD src0_sel:WORD_1 src1_sel:DWORD
	v_add3_u32 v203, v32, v203, s71
	v_and_b32_sdwa v32, v201, v198 dst_sel:DWORD dst_unused:UNUSED_PAD src0_sel:WORD_1 src1_sel:DWORD
	v_add3_u32 v202, v33, v202, s71
	v_and_b32_sdwa v33, v200, v198 dst_sel:DWORD dst_unused:UNUSED_PAD src0_sel:WORD_1 src1_sel:DWORD
	v_add3_u32 v201, v201, v32, s71
	v_lshl_add_u64 v[30:31], v[10:11], 0, s[56:57]
	v_add3_u32 v200, v200, v33, s71
	v_and_b32_e32 v201, 0xffff0000, v201
	v_and_b32_e32 v200, 0xffff0000, v200
	v_or_b32_sdwa v201, v201, v202 dst_sel:DWORD dst_unused:UNUSED_PAD src0_sel:DWORD src1_sel:WORD_1
	v_add_co_u32_e32 v202, vcc, s72, v30
	v_or_b32_sdwa v200, v200, v203 dst_sel:DWORD dst_unused:UNUSED_PAD src0_sel:DWORD src1_sel:WORD_1
	s_nop 0
	v_addc_co_u32_e32 v203, vcc, 0, v31, vcc
	global_store_dwordx2 v[202:203], v[200:201], off offset:3072
	v_lshlrev_b32_e32 v201, 16, v207
	v_lshlrev_b32_e32 v200, 16, v206
	v_pk_mul_f32 v[200:201], v[28:29], v[200:201] op_sel_hi:[0,1]
	v_and_b32_e32 v207, 0xffff0000, v207
	v_and_b32_e32 v206, 0xffff0000, v206
	v_pk_mul_f32 v[200:201], v[4:5], v[200:201]
	v_lshlrev_b32_e32 v31, 16, v205
	v_lshlrev_b32_e32 v30, 16, v204
	v_pk_mul_f32 v[206:207], v[28:29], v[206:207] op_sel_hi:[0,1]
	v_pk_mul_f32 v[200:201], v[200:201], v[30:31]
	v_pk_mul_f32 v[206:207], v[2:3], v[206:207]
	v_and_b32_e32 v205, 0xffff0000, v205
	v_and_b32_e32 v204, 0xffff0000, v204
	v_pk_mul_f32 v[204:205], v[206:207], v[204:205]
	v_and_b32_sdwa v206, v201, v198 dst_sel:DWORD dst_unused:UNUSED_PAD src0_sel:WORD_1 src1_sel:DWORD
	v_and_b32_sdwa v207, v200, v198 dst_sel:DWORD dst_unused:UNUSED_PAD src0_sel:WORD_1 src1_sel:DWORD
	v_add3_u32 v200, v200, v207, s71
	v_add3_u32 v201, v201, v206, s71
	v_and_b32_sdwa v206, v205, v198 dst_sel:DWORD dst_unused:UNUSED_PAD src0_sel:WORD_1 src1_sel:DWORD
	v_and_b32_sdwa v207, v204, v198 dst_sel:DWORD dst_unused:UNUSED_PAD src0_sel:WORD_1 src1_sel:DWORD
	v_add3_u32 v205, v205, v206, s71
	v_add3_u32 v204, v204, v207, s71
	v_and_b32_e32 v205, 0xffff0000, v205
	v_and_b32_e32 v204, 0xffff0000, v204
	s_add_u32 s56, s56, 0x8000
	v_or_b32_sdwa v205, v205, v201 dst_sel:DWORD dst_unused:UNUSED_PAD src0_sel:DWORD src1_sel:WORD_1
	v_or_b32_sdwa v204, v204, v200 dst_sel:DWORD dst_unused:UNUSED_PAD src0_sel:DWORD src1_sel:WORD_1
	s_addc_u32 s57, s57, 0
	global_store_dwordx2 v[202:203], v[204:205], off offset:3104
	v_add_u32_e32 v29, 0x200, v29
	s_waitcnt vmcnt(14)
	v_add_u32_e32 v28, -16, v29
	ds_read_b128 v[30:33], v28
	ds_read_b128 v[34:37], v29
	s_mov_b32 s58, 0x800000
	s_waitcnt lgkmcnt(1)
	v_mov_b32_e32 v38, v31
	v_mov_b32_e32 v39, v32
	v_mov_b32_e32 v31, v33
	v_pk_add_f32 v[30:31], v[38:39], v[30:31]
	s_waitcnt lgkmcnt(0)
	v_mov_b32_e32 v32, v36
	v_mov_b32_e32 v33, v34
	v_mov_b32_e32 v34, v37
	v_pk_add_f32 v[32:33], v[32:33], v[34:35]
	v_add_f32_e32 v28, v30, v31
	v_add_f32_e32 v28, v28, v33
	v_add_f32_e32 v28, v32, v28
	v_fmamk_f32 v28, v28, 0x3b800000, v195
	v_cmp_gt_f32_e32 vcc, s58, v28
	v_mul_f32_e32 v30, 0x4b800000, v28
	v_lshlrev_b32_e32 v33, 16, v211
	v_cndmask_b32_e32 v28, v28, v30, vcc
	v_rsq_f32_e32 v28, v28
	v_lshlrev_b32_e32 v32, 16, v210
	v_and_b32_e32 v211, 0xffff0000, v211
	v_and_b32_e32 v210, 0xffff0000, v210
	v_mul_f32_e32 v30, 0x45800000, v28
	v_cndmask_b32_e32 v28, v28, v30, vcc
	v_pk_mul_f32 v[32:33], v[28:29], v[32:33] op_sel_hi:[0,1]
	v_pk_mul_f32 v[32:33], v[0:1], v[32:33]
	v_lshlrev_b32_e32 v35, 16, v209
	v_lshlrev_b32_e32 v34, 16, v208
	v_pk_mul_f32 v[210:211], v[28:29], v[210:211] op_sel_hi:[0,1]
	v_pk_mul_f32 v[32:33], v[32:33], v[34:35]
	v_pk_mul_f32 v[210:211], v[8:9], v[210:211]
	v_and_b32_e32 v209, 0xffff0000, v209
	v_and_b32_e32 v208, 0xffff0000, v208
	v_pk_mul_f32 v[208:209], v[210:211], v[208:209]
	v_and_b32_sdwa v211, v32, v198 dst_sel:DWORD dst_unused:UNUSED_PAD src0_sel:WORD_1 src1_sel:DWORD
	v_and_b32_sdwa v210, v33, v198 dst_sel:DWORD dst_unused:UNUSED_PAD src0_sel:WORD_1 src1_sel:DWORD
	v_add3_u32 v211, v32, v211, s71
	v_and_b32_sdwa v32, v209, v198 dst_sel:DWORD dst_unused:UNUSED_PAD src0_sel:WORD_1 src1_sel:DWORD
	v_add3_u32 v210, v33, v210, s71
	v_and_b32_sdwa v33, v208, v198 dst_sel:DWORD dst_unused:UNUSED_PAD src0_sel:WORD_1 src1_sel:DWORD
	v_add3_u32 v209, v209, v32, s71
	v_lshl_add_u64 v[30:31], v[10:11], 0, s[56:57]
	v_add3_u32 v208, v208, v33, s71
	v_and_b32_e32 v209, 0xffff0000, v209
	v_and_b32_e32 v208, 0xffff0000, v208
	v_or_b32_sdwa v209, v209, v210 dst_sel:DWORD dst_unused:UNUSED_PAD src0_sel:DWORD src1_sel:WORD_1
	v_add_co_u32_e32 v210, vcc, s72, v30
	v_or_b32_sdwa v208, v208, v211 dst_sel:DWORD dst_unused:UNUSED_PAD src0_sel:DWORD src1_sel:WORD_1
	s_nop 0
	v_addc_co_u32_e32 v211, vcc, 0, v31, vcc
	global_store_dwordx2 v[210:211], v[208:209], off offset:3072
	v_lshlrev_b32_e32 v209, 16, v215
	v_lshlrev_b32_e32 v208, 16, v214
	v_pk_mul_f32 v[208:209], v[28:29], v[208:209] op_sel_hi:[0,1]
	v_and_b32_e32 v215, 0xffff0000, v215
	v_and_b32_e32 v214, 0xffff0000, v214
	v_pk_mul_f32 v[208:209], v[4:5], v[208:209]
	v_lshlrev_b32_e32 v31, 16, v213
	v_lshlrev_b32_e32 v30, 16, v212
	v_pk_mul_f32 v[214:215], v[28:29], v[214:215] op_sel_hi:[0,1]
	v_pk_mul_f32 v[208:209], v[208:209], v[30:31]
	v_pk_mul_f32 v[214:215], v[2:3], v[214:215]
	v_and_b32_e32 v213, 0xffff0000, v213
	v_and_b32_e32 v212, 0xffff0000, v212
	v_pk_mul_f32 v[212:213], v[214:215], v[212:213]
	v_and_b32_sdwa v214, v209, v198 dst_sel:DWORD dst_unused:UNUSED_PAD src0_sel:WORD_1 src1_sel:DWORD
	v_and_b32_sdwa v215, v208, v198 dst_sel:DWORD dst_unused:UNUSED_PAD src0_sel:WORD_1 src1_sel:DWORD
	v_add3_u32 v208, v208, v215, s71
	v_add3_u32 v209, v209, v214, s71
	v_and_b32_sdwa v214, v213, v198 dst_sel:DWORD dst_unused:UNUSED_PAD src0_sel:WORD_1 src1_sel:DWORD
	v_and_b32_sdwa v215, v212, v198 dst_sel:DWORD dst_unused:UNUSED_PAD src0_sel:WORD_1 src1_sel:DWORD
	v_add3_u32 v213, v213, v214, s71
	v_add3_u32 v212, v212, v215, s71
	v_and_b32_e32 v213, 0xffff0000, v213
	v_and_b32_e32 v212, 0xffff0000, v212
	s_add_u32 s56, s56, 0x8000
	v_or_b32_sdwa v213, v213, v209 dst_sel:DWORD dst_unused:UNUSED_PAD src0_sel:DWORD src1_sel:WORD_1
	v_or_b32_sdwa v212, v212, v208 dst_sel:DWORD dst_unused:UNUSED_PAD src0_sel:DWORD src1_sel:WORD_1
	s_addc_u32 s57, s57, 0
	global_store_dwordx2 v[210:211], v[212:213], off offset:3104
	v_add_u32_e32 v29, 0x200, v29
	v_readlane_b32 s49, v253, 63
	s_add_i32 s52, s52, s49
	s_add_i32 s63, s63, s64
	s_cmpk_lt_i32 s52, 0x200
	s_barrier
	s_cbranch_scc1 .LBB0_759
	v_readlane_b32 s64, v253, 45
	v_readlane_b32 s48, v252, 16
	v_readlane_b32 s2, v252, 14
	v_readlane_b32 s68, v253, 49
	v_readlane_b32 s69, v253, 50
	v_readlane_b32 s72, v253, 53
	v_readlane_b32 s73, v253, 54
	v_readlane_b32 s84, v253, 63
	v_readlane_b32 s85, v252, 0
	v_readlane_b32 s86, v252, 1
	v_readlane_b32 s87, v252, 2
	v_readlane_b32 s90, v252, 3
	v_readlane_b32 s49, v252, 17
	v_readlane_b32 s3, v252, 15
	v_readlane_b32 s65, v253, 46
	v_readlane_b32 s66, v253, 47
	v_readlane_b32 s67, v253, 48
	v_readlane_b32 s70, v253, 51
	v_readlane_b32 s71, v253, 52
	v_readlane_b32 s74, v253, 55
	v_readlane_b32 s75, v253, 56
	v_readlane_b32 s76, v253, 57
	v_readlane_b32 s77, v253, 58
	v_readlane_b32 s78, v253, 59
	v_readlane_b32 s79, v253, 60

.LBB0_870:
	global_load_dwordx4 v[204:207], v[178:179], off
	global_load_dwordx4 v[208:211], v[144:145], off
	global_load_dwordx4 v[212:215], v[178:179], off offset:256
	global_load_dwordx4 v[216:219], v[144:145], off offset:256
	global_load_dwordx4 v[140:143], v[180:181], off
	global_load_dwordx4 v[132:135], v[180:181], off offset:256
	global_load_dwordx4 v[136:139], v[146:147], off
	global_load_dwordx4 v[128:131], v[146:147], off offset:256
	s_waitcnt vmcnt(7)
	v_lshlrev_b32_e32 v220, 16, v204
	v_and_b32_e32 v204, 0xffff0000, v204
	v_lshlrev_b32_e32 v221, 16, v205
	v_lshlrev_b32_e32 v222, 16, v206
	v_lshlrev_b32_e32 v223, 16, v207
	v_and_b32_e32 v226, 0xffff0000, v207
	s_waitcnt vmcnt(6)
	v_lshlrev_b32_e32 v207, 16, v208
	v_and_b32_e32 v208, 0xffff0000, v208
	v_lshlrev_b32_e32 v224, 16, v209
	v_and_b32_e32 v209, 0xffff0000, v209
	v_lshlrev_b32_e32 v225, 16, v210
	v_and_b32_e32 v210, 0xffff0000, v210
	v_and_b32_e32 v205, 0xffff0000, v205
	v_and_b32_e32 v206, 0xffff0000, v206
	v_mul_f32_e32 v204, 0xbfb8aa3b, v204
	v_mul_f32_e32 v208, 0xbfb8aa3b, v208
	v_mul_f32_e32 v221, 0xbfb8aa3b, v221
	v_mul_f32_e32 v224, 0xbfb8aa3b, v224
	v_mul_f32_e32 v209, 0xbfb8aa3b, v209
	v_mul_f32_e32 v222, 0xbfb8aa3b, v222
	v_mul_f32_e32 v225, 0xbfb8aa3b, v225
	v_mul_f32_e32 v210, 0xbfb8aa3b, v210
	v_mul_f32_e32 v205, 0xbfb8aa3b, v205
	v_mul_f32_e32 v206, 0xbfb8aa3b, v206
	v_exp_f32_e32 v204, v204
	v_exp_f32_e32 v208, v208
	v_exp_f32_e32 v221, v221
	v_exp_f32_e32 v224, v224
	v_exp_f32_e32 v209, v209
	v_exp_f32_e32 v222, v222
	v_exp_f32_e32 v225, v225
	v_exp_f32_e32 v210, v210
	v_exp_f32_e32 v205, v205
	v_exp_f32_e32 v206, v206
	v_mul_f32_e32 v220, 0xbfb8aa3b, v220
	v_mul_f32_e32 v207, 0xbfb8aa3b, v207
	v_mul_f32_e32 v223, 0xbfb8aa3b, v223
	v_exp_f32_e32 v220, v220
	v_exp_f32_e32 v207, v207
	v_exp_f32_e32 v223, v223
	v_add_f32_e32 v228, 1.0, v204
	v_add_f32_e32 v208, 1.0, v208
	v_add_f32_e32 v221, 1.0, v221
	v_add_f32_e32 v224, 1.0, v224
	v_add_f32_e32 v209, 1.0, v209
	v_add_f32_e32 v222, 1.0, v222
	v_add_f32_e32 v225, 1.0, v225
	v_add_f32_e32 v210, 1.0, v210
	v_lshlrev_b32_e32 v227, 16, v211
	v_add_f32_e32 v229, 1.0, v205
	v_add_f32_e32 v230, 1.0, v206
	v_rcp_f32_e32 v205, v228
	v_min_f32_e32 v228, 0x49800000, v208
	v_rcp_f32_e32 v206, v221
	v_min_f32_e32 v221, 0x49800000, v224
	v_min_f32_e32 v224, 0x49800000, v209
	v_rcp_f32_e32 v208, v222
	v_min_f32_e32 v222, 0x49800000, v225
	v_min_f32_e32 v225, 0x49800000, v210
	v_and_b32_e32 v211, 0xffff0000, v211
	v_mul_f32_e32 v227, 0xbfb8aa3b, v227
	v_mul_f32_e32 v211, 0xbfb8aa3b, v211
	v_exp_f32_e32 v227, v227
	v_add_f32_e32 v220, 1.0, v220
	v_add_f32_e32 v207, 1.0, v207
	v_add_f32_e32 v223, 1.0, v223
	v_exp_f32_e32 v211, v211
	v_rcp_f32_e32 v204, v220
	v_min_f32_e32 v220, 0x49800000, v207
	v_rcp_f32_e32 v207, v229
	v_rcp_f32_e32 v210, v223
	v_mov_b32_e32 v223, v228
	v_mov_b32_e32 v229, v222
	v_rcp_f32_e32 v209, v230
	v_mov_b32_e32 v228, v221
	v_mov_b32_e32 v221, v223
	v_mov_b32_e32 v223, v224
	v_mov_b32_e32 v224, v229
	v_add_f32_e32 v227, 1.0, v227
	v_min_f32_e32 v227, 0x49800000, v227
	v_mul_f32_e32 v226, 0xbfb8aa3b, v226
	v_add_f32_e32 v211, 1.0, v211
	v_mov_b32_e32 v222, v228
	v_exp_f32_e32 v228, v226
	v_min_f32_e32 v229, 0x49800000, v211
	v_pk_mul_f32 v[208:209], v[208:209], v[224:225]
	v_pk_mul_f32 v[120:121], v[120:121], v[208:209]
	s_waitcnt vmcnt(4)
	v_and_b32_e32 v208, 0xffff0000, v216
	v_mul_f32_e32 v208, 0xbfb8aa3b, v208
	v_mov_b32_e32 v226, v227
	v_add_f32_e32 v211, 1.0, v228
	v_mov_b32_e32 v227, v229
	v_exp_f32_e32 v208, v208
	v_rcp_f32_e32 v211, v211
	v_pk_mul_f32 v[204:205], v[204:205], v[220:221]
	v_pk_mul_f32 v[206:207], v[206:207], v[222:223]
	v_pk_mul_f32 v[124:125], v[124:125], v[204:205]
	v_lshlrev_b32_e32 v204, 16, v212
	v_and_b32_e32 v205, 0xffff0000, v212
	v_and_b32_e32 v212, 0xffff0000, v217
	v_mul_f32_e32 v212, 0xbfb8aa3b, v212
	v_pk_mul_f32 v[126:127], v[126:127], v[206:207]
	v_lshlrev_b32_e32 v207, 16, v213
	v_add_f32_e32 v208, 1.0, v208
	v_exp_f32_e32 v212, v212
	v_pk_mul_f32 v[210:211], v[210:211], v[226:227]
	v_min_f32_e32 v208, 0x49800000, v208
	v_mul_f32_e32 v207, 0xbfb8aa3b, v207
	v_pk_mul_f32 v[122:123], v[122:123], v[210:211]
	v_and_b32_e32 v209, 0xffff0000, v213
	v_lshlrev_b32_e32 v211, 16, v214
	v_and_b32_e32 v213, 0xffff0000, v214
	v_lshlrev_b32_e32 v220, 16, v215
	v_and_b32_e32 v221, 0xffff0000, v215
	v_lshlrev_b32_e32 v214, 16, v218
	v_and_b32_e32 v215, 0xffff0000, v218
	v_exp_f32_e32 v218, v207
	v_lshlrev_b32_e32 v210, 16, v217
	v_add_f32_e32 v212, 1.0, v212
	v_mul_f32_e32 v214, 0xbfb8aa3b, v214
	v_lshlrev_b32_e32 v206, 16, v216
	v_lshlrev_b32_e32 v216, 16, v219
	v_mul_f32_e32 v207, 0xbfb8aa3b, v210
	v_min_f32_e32 v212, 0x49800000, v212
	v_exp_f32_e32 v214, v214
	v_mul_f32_e32 v211, 0xbfb8aa3b, v211
	v_exp_f32_e32 v210, v207
	v_mov_b32_e32 v207, v208
	v_add_f32_e32 v208, 1.0, v218
	v_exp_f32_e32 v218, v211
	v_mul_f32_e32 v216, 0xbfb8aa3b, v216
	v_exp_f32_e32 v216, v216
	v_add_f32_e32 v211, 1.0, v214
	v_mul_f32_e32 v206, 0xbfb8aa3b, v206
	v_and_b32_e32 v217, 0xffff0000, v219
	v_min_f32_e32 v214, 0x49800000, v211
	v_mov_b32_e32 v211, v212
	v_add_f32_e32 v212, 1.0, v218
	v_mul_f32_e32 v218, 0xbfb8aa3b, v220
	v_exp_f32_e32 v206, v206
	v_mul_f32_e32 v215, 0xbfb8aa3b, v215
	v_exp_f32_e32 v218, v218
	v_add_f32_e32 v216, 1.0, v216
	v_mul_f32_e32 v217, 0xbfb8aa3b, v217
	v_exp_f32_e32 v215, v215
	v_min_f32_e32 v219, 0x49800000, v216
	v_exp_f32_e32 v217, v217
	v_mul_f32_e32 v204, 0xbfb8aa3b, v204
	v_add_f32_e32 v206, 1.0, v206
	v_mul_f32_e32 v205, 0xbfb8aa3b, v205
	v_add_f32_e32 v210, 1.0, v210
	v_mul_f32_e32 v209, 0xbfb8aa3b, v209
	v_add_f32_e32 v218, 1.0, v218
	v_exp_f32_e32 v204, v204
	v_min_f32_e32 v206, 0x49800000, v206
	v_exp_f32_e32 v205, v205
	v_min_f32_e32 v210, 0x49800000, v210
	v_exp_f32_e32 v209, v209
	v_mul_f32_e32 v213, 0xbfb8aa3b, v213
	v_add_f32_e32 v215, 1.0, v215
	v_rcp_f32_e32 v216, v218
	v_mov_b32_e32 v218, v219
	v_mul_f32_e32 v219, 0xbfb8aa3b, v221
	v_add_f32_e32 v217, 1.0, v217
	v_exp_f32_e32 v213, v213
	v_min_f32_e32 v215, 0x49800000, v215
	v_exp_f32_e32 v219, v219
	v_min_f32_e32 v220, 0x49800000, v217
	v_add_f32_e32 v204, 1.0, v204
	v_add_f32_e32 v205, 1.0, v205
	v_add_f32_e32 v209, 1.0, v209
	v_rcp_f32_e32 v204, v204
	v_rcp_f32_e32 v205, v205
	v_rcp_f32_e32 v208, v208
	v_rcp_f32_e32 v209, v209
	v_add_f32_e32 v213, 1.0, v213
	v_add_f32_e32 v217, 1.0, v219
	v_mov_b32_e32 v219, v220
	v_rcp_f32_e32 v212, v212
	v_rcp_f32_e32 v213, v213
	v_rcp_f32_e32 v217, v217
	v_pk_mul_f32 v[204:205], v[204:205], v[206:207]
	v_pk_mul_f32 v[206:207], v[208:209], v[210:211]
	v_pk_mul_f32 v[208:209], v[212:213], v[214:215]
	v_pk_mul_f32 v[210:211], v[216:217], v[218:219]
	v_pk_mul_f32 v[118:119], v[118:119], v[206:207]
	s_waitcnt vmcnt(3)
	v_lshlrev_b32_e32 v206, 16, v142
	v_and_b32_e32 v207, 0xffff0000, v142
	s_waitcnt vmcnt(1)
	v_lshlrev_b32_e32 v142, 16, v136
	v_pk_mul_f32 v[114:115], v[114:115], v[210:211]
	v_pk_mul_f32 v[112:113], v[112:113], v[208:209]
	v_lshlrev_b32_e32 v208, 16, v143
	v_and_b32_e32 v209, 0xffff0000, v143
	v_and_b32_e32 v143, 0xffff0000, v136
	v_lshlrev_b32_e32 v210, 16, v137
	v_and_b32_e32 v211, 0xffff0000, v137
	v_mul_f32_e32 v137, 0xbfb8aa3b, v142
	v_lshlrev_b32_e32 v212, 16, v138
	v_and_b32_e32 v213, 0xffff0000, v138
	v_exp_f32_e32 v137, v137
	v_mul_f32_e32 v138, 0xbfb8aa3b, v143
	v_exp_f32_e32 v138, v138
	v_pk_mul_f32 v[116:117], v[116:117], v[204:205]
	v_lshlrev_b32_e32 v204, 16, v140
	v_and_b32_e32 v140, 0xffff0000, v140
	v_add_f32_e32 v137, 1.0, v137
	v_mul_f32_e32 v136, 0xbfb8aa3b, v204
	v_lshlrev_b32_e32 v214, 16, v139
	v_and_b32_e32 v215, 0xffff0000, v139
	v_min_f32_e32 v137, 0x49800000, v137
	v_mul_f32_e32 v139, 0xbfb8aa3b, v140
	v_add_f32_e32 v138, 1.0, v138
	v_mul_f32_e32 v204, 0xbfb8aa3b, v212
	v_exp_f32_e32 v139, v139
	v_min_f32_e32 v140, 0x49800000, v138
	v_exp_f32_e32 v204, v204
	v_lshlrev_b32_e32 v205, 16, v141
	v_mov_b32_e32 v138, v137
	v_add_f32_e32 v137, 1.0, v139
	v_mov_b32_e32 v139, v140
	v_mul_f32_e32 v140, 0xbfb8aa3b, v205
	v_mul_f32_e32 v205, 0xbfb8aa3b, v206
	v_add_f32_e32 v204, 1.0, v204
	v_exp_f32_e32 v205, v205
	v_min_f32_e32 v206, 0x49800000, v204
	v_mul_f32_e32 v142, 0xbfb8aa3b, v210
	v_mul_f32_e32 v143, 0xbfb8aa3b, v211
	v_add_f32_e32 v204, 1.0, v205
	v_mov_b32_e32 v205, v206
	v_mul_f32_e32 v206, 0xbfb8aa3b, v207
	v_exp_f32_e32 v207, v206
	v_mul_f32_e32 v206, 0xbfb8aa3b, v213
	v_exp_f32_e32 v210, v206
	v_mov_b32_e32 v206, v205
	v_add_f32_e32 v205, 1.0, v207
	v_mul_f32_e32 v211, 0xbfb8aa3b, v215
	v_add_f32_e32 v207, 1.0, v210
	v_mul_f32_e32 v210, 0xbfb8aa3b, v214
	v_exp_f32_e32 v142, v142
	v_exp_f32_e32 v143, v143
	v_exp_f32_e32 v210, v210
	v_exp_f32_e32 v211, v211
	v_and_b32_e32 v141, 0xffff0000, v141
	v_add_f32_e32 v142, 1.0, v142
	v_mul_f32_e32 v141, 0xbfb8aa3b, v141
	v_add_f32_e32 v143, 1.0, v143
	v_mul_f32_e32 v208, 0xbfb8aa3b, v208
	v_add_f32_e32 v210, 1.0, v210
	v_mul_f32_e32 v209, 0xbfb8aa3b, v209
	v_add_f32_e32 v211, 1.0, v211
	v_exp_f32_e32 v136, v136
	v_exp_f32_e32 v140, v140
	v_min_f32_e32 v142, 0x49800000, v142
	v_exp_f32_e32 v141, v141
	v_min_f32_e32 v143, 0x49800000, v143
	v_min_f32_e32 v207, 0x49800000, v207
	v_exp_f32_e32 v208, v208
	v_min_f32_e32 v210, 0x49800000, v210
	v_exp_f32_e32 v209, v209
	v_min_f32_e32 v211, 0x49800000, v211
	v_add_f32_e32 v136, 1.0, v136
	v_add_f32_e32 v140, 1.0, v140
	v_add_f32_e32 v141, 1.0, v141
	v_add_f32_e32 v208, 1.0, v208
	v_add_f32_e32 v209, 1.0, v209
	v_rcp_f32_e32 v136, v136
	v_rcp_f32_e32 v137, v137
	v_rcp_f32_e32 v140, v140
	v_rcp_f32_e32 v141, v141
	v_rcp_f32_e32 v204, v204
	v_rcp_f32_e32 v205, v205
	v_rcp_f32_e32 v208, v208
	v_rcp_f32_e32 v209, v209
	v_pk_mul_f32 v[136:137], v[136:137], v[138:139]
	v_pk_mul_f32 v[138:139], v[140:141], v[142:143]
	v_pk_mul_f32 v[140:141], v[204:205], v[206:207]
	v_pk_mul_f32 v[142:143], v[208:209], v[210:211]
	global_load_dwordx4 v[204:207], v[182:183], off
	global_load_dwordx4 v[208:211], v[174:175], off
	v_pk_mul_f32 v[110:111], v[110:111], v[138:139]
	v_lshlrev_b32_e32 v138, 16, v134
	v_and_b32_e32 v139, 0xffff0000, v134
	s_waitcnt vmcnt(2)
	v_lshlrev_b32_e32 v134, 16, v128
	v_pk_mul_f32 v[104:105], v[104:105], v[140:141]
	v_lshlrev_b32_e32 v140, 16, v135
	v_and_b32_e32 v141, 0xffff0000, v135
	v_and_b32_e32 v135, 0xffff0000, v128
	v_mul_f32_e32 v128, 0xbfb8aa3b, v134
	v_exp_f32_e32 v128, v128
	v_pk_mul_f32 v[108:109], v[108:109], v[136:137]
	v_lshlrev_b32_e32 v136, 16, v132
	v_pk_mul_f32 v[106:107], v[106:107], v[142:143]
	v_lshlrev_b32_e32 v142, 16, v129
	v_and_b32_e32 v143, 0xffff0000, v129
	v_lshlrev_b32_e32 v212, 16, v130
	v_mul_f32_e32 v129, 0xbfb8aa3b, v136
	v_add_f32_e32 v128, 1.0, v128
	v_and_b32_e32 v213, 0xffff0000, v130
	v_exp_f32_e32 v129, v129
	v_min_f32_e32 v130, 0x49800000, v128
	v_mul_f32_e32 v136, 0xbfb8aa3b, v212
	v_exp_f32_e32 v136, v136
	v_and_b32_e32 v132, 0xffff0000, v132
	v_lshlrev_b32_e32 v137, 16, v133
	v_add_f32_e32 v128, 1.0, v129
	v_mov_b32_e32 v129, v130
	v_mul_f32_e32 v130, 0xbfb8aa3b, v135
	v_lshlrev_b32_e32 v214, 16, v131
	v_and_b32_e32 v215, 0xffff0000, v131
	v_exp_f32_e32 v131, v130
	v_mov_b32_e32 v130, v129
	v_mul_f32_e32 v129, 0xbfb8aa3b, v132
	v_mul_f32_e32 v132, 0xbfb8aa3b, v137
	v_mul_f32_e32 v137, 0xbfb8aa3b, v138
	v_add_f32_e32 v136, 1.0, v136
	v_exp_f32_e32 v137, v137
	v_min_f32_e32 v138, 0x49800000, v136
	v_mul_f32_e32 v134, 0xbfb8aa3b, v142
	v_mul_f32_e32 v135, 0xbfb8aa3b, v143
	v_add_f32_e32 v136, 1.0, v137
	v_mov_b32_e32 v137, v138
	v_mul_f32_e32 v138, 0xbfb8aa3b, v139
	v_exp_f32_e32 v139, v138
	v_mul_f32_e32 v138, 0xbfb8aa3b, v213
	v_exp_f32_e32 v142, v138
	v_mov_b32_e32 v138, v137
	v_add_f32_e32 v137, 1.0, v139
	v_mul_f32_e32 v143, 0xbfb8aa3b, v215
	v_add_f32_e32 v139, 1.0, v142
	v_mul_f32_e32 v142, 0xbfb8aa3b, v214
	v_exp_f32_e32 v134, v134
	v_exp_f32_e32 v135, v135
	v_exp_f32_e32 v142, v142
	v_exp_f32_e32 v143, v143
	v_and_b32_e32 v133, 0xffff0000, v133
	v_add_f32_e32 v131, 1.0, v131
	v_add_f32_e32 v134, 1.0, v134
	v_mul_f32_e32 v133, 0xbfb8aa3b, v133
	v_add_f32_e32 v135, 1.0, v135
	v_mul_f32_e32 v140, 0xbfb8aa3b, v140
	v_add_f32_e32 v142, 1.0, v142
	v_mul_f32_e32 v141, 0xbfb8aa3b, v141
	v_add_f32_e32 v143, 1.0, v143
	v_exp_f32_e32 v129, v129
	v_min_f32_e32 v131, 0x49800000, v131
	v_exp_f32_e32 v132, v132
	v_min_f32_e32 v134, 0x49800000, v134
	v_exp_f32_e32 v133, v133
	v_min_f32_e32 v135, 0x49800000, v135
	v_min_f32_e32 v139, 0x49800000, v139
	v_exp_f32_e32 v140, v140
	v_min_f32_e32 v142, 0x49800000, v142
	v_exp_f32_e32 v141, v141
	v_min_f32_e32 v143, 0x49800000, v143
	v_add_f32_e32 v129, 1.0, v129
	v_add_f32_e32 v132, 1.0, v132
	v_add_f32_e32 v133, 1.0, v133
	v_add_f32_e32 v140, 1.0, v140
	v_add_f32_e32 v141, 1.0, v141
	v_rcp_f32_e32 v128, v128
	v_rcp_f32_e32 v129, v129
	v_rcp_f32_e32 v132, v132
	v_rcp_f32_e32 v133, v133
	v_rcp_f32_e32 v136, v136
	v_rcp_f32_e32 v137, v137
	v_rcp_f32_e32 v140, v140
	v_rcp_f32_e32 v141, v141
	v_pk_mul_f32 v[128:129], v[128:129], v[130:131]
	v_pk_mul_f32 v[130:131], v[132:133], v[134:135]
	v_pk_mul_f32 v[132:133], v[136:137], v[138:139]
	v_pk_mul_f32 v[134:135], v[140:141], v[142:143]
	v_pk_mul_f32 v[102:103], v[102:103], v[130:131]
	v_pk_mul_f32 v[100:101], v[100:101], v[128:129]
	v_pk_mul_f32 v[98:99], v[98:99], v[134:135]
	v_pk_mul_f32 v[96:97], v[96:97], v[132:133]
	global_load_dwordx4 v[212:215], v[182:183], off offset:256
	global_load_dwordx4 v[216:219], v[174:175], off offset:256
	global_load_dwordx4 v[140:143], v[184:185], off
	global_load_dwordx4 v[132:135], v[184:185], off offset:256
	global_load_dwordx4 v[136:139], v[176:177], off
	global_load_dwordx4 v[128:131], v[176:177], off offset:256
	s_waitcnt vmcnt(7)
	v_lshlrev_b32_e32 v220, 16, v204
	v_and_b32_e32 v221, 0xffff0000, v204
	s_waitcnt vmcnt(6)
	v_lshlrev_b32_e32 v204, 16, v208
	v_mul_f32_e32 v204, 0xbfb8aa3b, v204
	v_exp_f32_e32 v204, v204
	v_lshlrev_b32_e32 v222, 16, v205
	v_and_b32_e32 v223, 0xffff0000, v205
	v_lshlrev_b32_e32 v224, 16, v206
	v_and_b32_e32 v225, 0xffff0000, v206
	v_and_b32_e32 v205, 0xffff0000, v208
	v_mul_f32_e32 v206, 0xbfb8aa3b, v220
	v_exp_f32_e32 v206, v206
	v_add_f32_e32 v204, 1.0, v204
	v_mul_f32_e32 v205, 0xbfb8aa3b, v205
	v_min_f32_e32 v208, 0x49800000, v204
	v_exp_f32_e32 v205, v205
	v_add_f32_e32 v206, 1.0, v206
	v_rcp_f32_e32 v204, v206
	v_mov_b32_e32 v206, v208
	v_mul_f32_e32 v208, 0xbfb8aa3b, v221
	v_add_f32_e32 v205, 1.0, v205
	v_lshlrev_b32_e32 v228, 16, v210
	v_and_b32_e32 v229, 0xffff0000, v210
	v_exp_f32_e32 v208, v208
	v_min_f32_e32 v210, 0x49800000, v205
	v_lshlrev_b32_e32 v226, 16, v207
	v_and_b32_e32 v227, 0xffff0000, v207
	v_lshlrev_b32_e32 v207, 16, v209
	v_add_f32_e32 v205, 1.0, v208
	v_mov_b32_e32 v208, v210
	v_mul_f32_e32 v210, 0xbfb8aa3b, v222
	v_mul_f32_e32 v207, 0xbfb8aa3b, v207
	v_lshlrev_b32_e32 v230, 16, v211
	v_and_b32_e32 v231, 0xffff0000, v211
	v_exp_f32_e32 v210, v210
	v_exp_f32_e32 v211, v207
	v_and_b32_e32 v209, 0xffff0000, v209
	v_mov_b32_e32 v207, v208
	v_add_f32_e32 v208, 1.0, v210
	v_add_f32_e32 v210, 1.0, v211
	v_mul_f32_e32 v211, 0xbfb8aa3b, v223
	v_mul_f32_e32 v209, 0xbfb8aa3b, v209
	v_exp_f32_e32 v211, v211
	v_exp_f32_e32 v209, v209
	v_mul_f32_e32 v221, 0xbfb8aa3b, v224
	v_exp_f32_e32 v221, v221
	v_add_f32_e32 v211, 1.0, v211
	v_add_f32_e32 v209, 1.0, v209
	v_min_f32_e32 v220, 0x49800000, v209
	v_rcp_f32_e32 v209, v211
	v_mul_f32_e32 v211, 0xbfb8aa3b, v228
	v_exp_f32_e32 v211, v211
	v_min_f32_e32 v210, 0x49800000, v210
	v_add_f32_e32 v211, 1.0, v211
	v_min_f32_e32 v222, 0x49800000, v211
	v_mov_b32_e32 v211, v220
	v_add_f32_e32 v220, 1.0, v221
	v_mov_b32_e32 v221, v222
	v_mul_f32_e32 v222, 0xbfb8aa3b, v225
	v_exp_f32_e32 v223, v222
	v_mul_f32_e32 v222, 0xbfb8aa3b, v229
	v_exp_f32_e32 v224, v222
	v_mov_b32_e32 v222, v221
	v_add_f32_e32 v221, 1.0, v223
	v_mul_f32_e32 v225, 0xbfb8aa3b, v230
	v_add_f32_e32 v223, 1.0, v224
	v_min_f32_e32 v223, 0x49800000, v223
	v_mul_f32_e32 v224, 0xbfb8aa3b, v226
	v_exp_f32_e32 v225, v225
	v_mul_f32_e32 v226, 0xbfb8aa3b, v231
	v_exp_f32_e32 v226, v226
	v_rcp_f32_e32 v205, v205
	v_rcp_f32_e32 v208, v208
	v_rcp_f32_e32 v220, v220
	v_rcp_f32_e32 v221, v221
	v_add_f32_e32 v225, 1.0, v225
	v_min_f32_e32 v225, 0x49800000, v225
	v_mul_f32_e32 v227, 0xbfb8aa3b, v227
	v_add_f32_e32 v226, 1.0, v226
	v_exp_f32_e32 v224, v224
	v_exp_f32_e32 v227, v227
	v_min_f32_e32 v228, 0x49800000, v226
	v_pk_mul_f32 v[204:205], v[204:205], v[206:207]
	v_pk_mul_f32 v[206:207], v[208:209], v[210:211]
	v_pk_mul_f32 v[208:209], v[220:221], v[222:223]
	v_pk_mul_f32 v[88:89], v[88:89], v[208:209]
	s_waitcnt vmcnt(4)
	v_and_b32_e32 v208, 0xffff0000, v216
	v_mul_f32_e32 v208, 0xbfb8aa3b, v208
	v_add_f32_e32 v224, 1.0, v224
	v_mov_b32_e32 v226, v225
	v_add_f32_e32 v225, 1.0, v227
	v_mov_b32_e32 v227, v228
	v_exp_f32_e32 v208, v208
	v_rcp_f32_e32 v224, v224
	v_rcp_f32_e32 v225, v225
	v_pk_mul_f32 v[92:93], v[92:93], v[204:205]
	v_lshlrev_b32_e32 v204, 16, v212
	v_and_b32_e32 v205, 0xffff0000, v212
	v_and_b32_e32 v212, 0xffff0000, v217
	v_mul_f32_e32 v212, 0xbfb8aa3b, v212
	v_pk_mul_f32 v[94:95], v[94:95], v[206:207]
	v_lshlrev_b32_e32 v207, 16, v213
	v_add_f32_e32 v208, 1.0, v208
	v_exp_f32_e32 v212, v212
	v_pk_mul_f32 v[210:211], v[224:225], v[226:227]
	v_min_f32_e32 v208, 0x49800000, v208
	v_mul_f32_e32 v207, 0xbfb8aa3b, v207
	v_pk_mul_f32 v[90:91], v[90:91], v[210:211]
	v_and_b32_e32 v209, 0xffff0000, v213
	v_lshlrev_b32_e32 v211, 16, v214
	v_and_b32_e32 v213, 0xffff0000, v214
	v_lshlrev_b32_e32 v220, 16, v215
	v_and_b32_e32 v221, 0xffff0000, v215
	v_lshlrev_b32_e32 v214, 16, v218
	v_and_b32_e32 v215, 0xffff0000, v218
	v_exp_f32_e32 v218, v207
	v_lshlrev_b32_e32 v210, 16, v217
	v_add_f32_e32 v212, 1.0, v212
	v_mul_f32_e32 v214, 0xbfb8aa3b, v214
	v_lshlrev_b32_e32 v206, 16, v216
	v_lshlrev_b32_e32 v216, 16, v219
	v_mul_f32_e32 v207, 0xbfb8aa3b, v210
	v_min_f32_e32 v212, 0x49800000, v212
	v_exp_f32_e32 v214, v214
	v_mul_f32_e32 v211, 0xbfb8aa3b, v211
	v_exp_f32_e32 v210, v207
	v_mov_b32_e32 v207, v208
	v_add_f32_e32 v208, 1.0, v218
	v_exp_f32_e32 v218, v211
	v_mul_f32_e32 v216, 0xbfb8aa3b, v216
	v_exp_f32_e32 v216, v216
	v_add_f32_e32 v211, 1.0, v214
	v_mul_f32_e32 v206, 0xbfb8aa3b, v206
	v_and_b32_e32 v217, 0xffff0000, v219
	v_min_f32_e32 v214, 0x49800000, v211
	v_mov_b32_e32 v211, v212
	v_add_f32_e32 v212, 1.0, v218
	v_mul_f32_e32 v218, 0xbfb8aa3b, v220
	v_exp_f32_e32 v206, v206
	v_mul_f32_e32 v215, 0xbfb8aa3b, v215
	v_exp_f32_e32 v218, v218
	v_add_f32_e32 v216, 1.0, v216
	v_mul_f32_e32 v217, 0xbfb8aa3b, v217
	v_exp_f32_e32 v215, v215
	v_min_f32_e32 v219, 0x49800000, v216
	v_exp_f32_e32 v217, v217
	v_mul_f32_e32 v204, 0xbfb8aa3b, v204
	v_add_f32_e32 v206, 1.0, v206
	v_mul_f32_e32 v205, 0xbfb8aa3b, v205
	v_add_f32_e32 v210, 1.0, v210
	v_mul_f32_e32 v209, 0xbfb8aa3b, v209
	v_add_f32_e32 v218, 1.0, v218
	v_exp_f32_e32 v204, v204
	v_min_f32_e32 v206, 0x49800000, v206
	v_exp_f32_e32 v205, v205
	v_min_f32_e32 v210, 0x49800000, v210
	v_exp_f32_e32 v209, v209
	v_mul_f32_e32 v213, 0xbfb8aa3b, v213
	v_add_f32_e32 v215, 1.0, v215
	v_rcp_f32_e32 v216, v218
	v_mov_b32_e32 v218, v219
	v_mul_f32_e32 v219, 0xbfb8aa3b, v221
	v_add_f32_e32 v217, 1.0, v217
	v_exp_f32_e32 v213, v213
	v_min_f32_e32 v215, 0x49800000, v215
	v_exp_f32_e32 v219, v219
	v_min_f32_e32 v220, 0x49800000, v217
	v_add_f32_e32 v204, 1.0, v204
	v_add_f32_e32 v205, 1.0, v205
	v_add_f32_e32 v209, 1.0, v209
	v_rcp_f32_e32 v204, v204
	v_rcp_f32_e32 v205, v205
	v_rcp_f32_e32 v208, v208
	v_rcp_f32_e32 v209, v209
	v_add_f32_e32 v213, 1.0, v213
	v_add_f32_e32 v217, 1.0, v219
	v_mov_b32_e32 v219, v220
	v_rcp_f32_e32 v212, v212
	v_rcp_f32_e32 v213, v213
	v_rcp_f32_e32 v217, v217
	v_pk_mul_f32 v[204:205], v[204:205], v[206:207]
	v_pk_mul_f32 v[206:207], v[208:209], v[210:211]
	v_pk_mul_f32 v[208:209], v[212:213], v[214:215]
	v_pk_mul_f32 v[210:211], v[216:217], v[218:219]
	v_pk_mul_f32 v[86:87], v[86:87], v[206:207]
	s_waitcnt vmcnt(3)
	v_lshlrev_b32_e32 v206, 16, v142
	v_and_b32_e32 v207, 0xffff0000, v142
	s_waitcnt vmcnt(1)
	v_lshlrev_b32_e32 v142, 16, v136
	v_pk_mul_f32 v[82:83], v[82:83], v[210:211]
	v_pk_mul_f32 v[80:81], v[80:81], v[208:209]
	v_lshlrev_b32_e32 v208, 16, v143
	v_and_b32_e32 v209, 0xffff0000, v143
	v_and_b32_e32 v143, 0xffff0000, v136
	v_lshlrev_b32_e32 v210, 16, v137
	v_and_b32_e32 v211, 0xffff0000, v137
	v_mul_f32_e32 v137, 0xbfb8aa3b, v142
	v_lshlrev_b32_e32 v212, 16, v138
	v_and_b32_e32 v213, 0xffff0000, v138
	v_exp_f32_e32 v137, v137
	v_mul_f32_e32 v138, 0xbfb8aa3b, v143
	v_exp_f32_e32 v138, v138
	v_pk_mul_f32 v[84:85], v[84:85], v[204:205]
	v_lshlrev_b32_e32 v204, 16, v140
	v_and_b32_e32 v140, 0xffff0000, v140
	v_add_f32_e32 v137, 1.0, v137
	v_mul_f32_e32 v136, 0xbfb8aa3b, v204
	v_lshlrev_b32_e32 v214, 16, v139
	v_and_b32_e32 v215, 0xffff0000, v139
	v_min_f32_e32 v137, 0x49800000, v137
	v_mul_f32_e32 v139, 0xbfb8aa3b, v140
	v_add_f32_e32 v138, 1.0, v138
	v_mul_f32_e32 v204, 0xbfb8aa3b, v212
	v_exp_f32_e32 v139, v139
	v_min_f32_e32 v140, 0x49800000, v138
	v_exp_f32_e32 v204, v204
	v_lshlrev_b32_e32 v205, 16, v141
	v_mov_b32_e32 v138, v137
	v_add_f32_e32 v137, 1.0, v139
	v_mov_b32_e32 v139, v140
	v_mul_f32_e32 v140, 0xbfb8aa3b, v205
	v_mul_f32_e32 v205, 0xbfb8aa3b, v206
	v_add_f32_e32 v204, 1.0, v204
	v_exp_f32_e32 v205, v205
	v_min_f32_e32 v206, 0x49800000, v204
	v_mul_f32_e32 v142, 0xbfb8aa3b, v210
	v_mul_f32_e32 v143, 0xbfb8aa3b, v211
	v_add_f32_e32 v204, 1.0, v205
	v_mov_b32_e32 v205, v206
	v_mul_f32_e32 v206, 0xbfb8aa3b, v207
	v_exp_f32_e32 v207, v206
	v_mul_f32_e32 v206, 0xbfb8aa3b, v213
	v_exp_f32_e32 v210, v206
	v_mov_b32_e32 v206, v205
	v_add_f32_e32 v205, 1.0, v207
	v_mul_f32_e32 v211, 0xbfb8aa3b, v215
	v_add_f32_e32 v207, 1.0, v210
	v_mul_f32_e32 v210, 0xbfb8aa3b, v214
	v_exp_f32_e32 v142, v142
	v_exp_f32_e32 v143, v143
	v_exp_f32_e32 v210, v210
	v_exp_f32_e32 v211, v211
	v_and_b32_e32 v141, 0xffff0000, v141
	v_add_f32_e32 v142, 1.0, v142
	v_mul_f32_e32 v141, 0xbfb8aa3b, v141
	v_add_f32_e32 v143, 1.0, v143
	v_mul_f32_e32 v208, 0xbfb8aa3b, v208
	v_add_f32_e32 v210, 1.0, v210
	v_mul_f32_e32 v209, 0xbfb8aa3b, v209
	v_add_f32_e32 v211, 1.0, v211
	v_exp_f32_e32 v136, v136
	v_exp_f32_e32 v140, v140
	v_min_f32_e32 v142, 0x49800000, v142
	v_exp_f32_e32 v141, v141
	v_min_f32_e32 v143, 0x49800000, v143
	v_min_f32_e32 v207, 0x49800000, v207
	v_exp_f32_e32 v208, v208
	v_min_f32_e32 v210, 0x49800000, v210
	v_exp_f32_e32 v209, v209
	v_min_f32_e32 v211, 0x49800000, v211
	v_add_f32_e32 v136, 1.0, v136
	v_add_f32_e32 v140, 1.0, v140
	v_add_f32_e32 v141, 1.0, v141
	v_add_f32_e32 v208, 1.0, v208
	v_add_f32_e32 v209, 1.0, v209
	v_rcp_f32_e32 v136, v136
	v_rcp_f32_e32 v137, v137
	v_rcp_f32_e32 v140, v140
	v_rcp_f32_e32 v141, v141
	v_rcp_f32_e32 v204, v204
	v_rcp_f32_e32 v205, v205
	v_rcp_f32_e32 v208, v208
	v_rcp_f32_e32 v209, v209
	v_pk_mul_f32 v[136:137], v[136:137], v[138:139]
	v_pk_mul_f32 v[138:139], v[140:141], v[142:143]
	v_pk_mul_f32 v[140:141], v[204:205], v[206:207]
	v_pk_mul_f32 v[142:143], v[208:209], v[210:211]
	global_load_dwordx4 v[204:207], v[186:187], off
	global_load_dwordx4 v[208:211], v[158:159], off
	v_pk_mul_f32 v[78:79], v[78:79], v[138:139]
	v_lshlrev_b32_e32 v138, 16, v134
	v_and_b32_e32 v139, 0xffff0000, v134
	s_waitcnt vmcnt(2)
	v_lshlrev_b32_e32 v134, 16, v128
	v_pk_mul_f32 v[72:73], v[72:73], v[140:141]
	v_lshlrev_b32_e32 v140, 16, v135
	v_and_b32_e32 v141, 0xffff0000, v135
	v_and_b32_e32 v135, 0xffff0000, v128
	v_mul_f32_e32 v128, 0xbfb8aa3b, v134
	v_exp_f32_e32 v128, v128
	v_pk_mul_f32 v[76:77], v[76:77], v[136:137]
	v_lshlrev_b32_e32 v136, 16, v132
	v_pk_mul_f32 v[74:75], v[74:75], v[142:143]
	v_lshlrev_b32_e32 v142, 16, v129
	v_and_b32_e32 v143, 0xffff0000, v129
	v_lshlrev_b32_e32 v212, 16, v130
	v_mul_f32_e32 v129, 0xbfb8aa3b, v136
	v_add_f32_e32 v128, 1.0, v128
	v_and_b32_e32 v213, 0xffff0000, v130
	v_exp_f32_e32 v129, v129
	v_min_f32_e32 v130, 0x49800000, v128
	v_mul_f32_e32 v136, 0xbfb8aa3b, v212
	v_exp_f32_e32 v136, v136
	v_and_b32_e32 v132, 0xffff0000, v132
	v_lshlrev_b32_e32 v137, 16, v133
	v_add_f32_e32 v128, 1.0, v129
	v_mov_b32_e32 v129, v130
	v_mul_f32_e32 v130, 0xbfb8aa3b, v135
	v_lshlrev_b32_e32 v214, 16, v131
	v_and_b32_e32 v215, 0xffff0000, v131
	v_exp_f32_e32 v131, v130
	v_mov_b32_e32 v130, v129
	v_mul_f32_e32 v129, 0xbfb8aa3b, v132
	v_mul_f32_e32 v132, 0xbfb8aa3b, v137
	v_mul_f32_e32 v137, 0xbfb8aa3b, v138
	v_add_f32_e32 v136, 1.0, v136
	v_exp_f32_e32 v137, v137
	v_min_f32_e32 v138, 0x49800000, v136
	v_mul_f32_e32 v134, 0xbfb8aa3b, v142
	v_mul_f32_e32 v135, 0xbfb8aa3b, v143
	v_add_f32_e32 v136, 1.0, v137
	v_mov_b32_e32 v137, v138
	v_mul_f32_e32 v138, 0xbfb8aa3b, v139
	v_exp_f32_e32 v139, v138
	v_mul_f32_e32 v138, 0xbfb8aa3b, v213
	v_exp_f32_e32 v142, v138
	v_mov_b32_e32 v138, v137
	v_add_f32_e32 v137, 1.0, v139
	v_mul_f32_e32 v143, 0xbfb8aa3b, v215
	v_add_f32_e32 v139, 1.0, v142
	v_mul_f32_e32 v142, 0xbfb8aa3b, v214
	v_exp_f32_e32 v134, v134
	v_exp_f32_e32 v135, v135
	v_exp_f32_e32 v142, v142
	v_exp_f32_e32 v143, v143
	v_and_b32_e32 v133, 0xffff0000, v133
	v_add_f32_e32 v131, 1.0, v131
	v_add_f32_e32 v134, 1.0, v134
	v_mul_f32_e32 v133, 0xbfb8aa3b, v133
	v_add_f32_e32 v135, 1.0, v135
	v_mul_f32_e32 v140, 0xbfb8aa3b, v140
	v_add_f32_e32 v142, 1.0, v142
	v_mul_f32_e32 v141, 0xbfb8aa3b, v141
	v_add_f32_e32 v143, 1.0, v143
	v_exp_f32_e32 v129, v129
	v_min_f32_e32 v131, 0x49800000, v131
	v_exp_f32_e32 v132, v132
	v_min_f32_e32 v134, 0x49800000, v134
	v_exp_f32_e32 v133, v133
	v_min_f32_e32 v135, 0x49800000, v135
	v_min_f32_e32 v139, 0x49800000, v139
	v_exp_f32_e32 v140, v140
	v_min_f32_e32 v142, 0x49800000, v142
	v_exp_f32_e32 v141, v141
	v_min_f32_e32 v143, 0x49800000, v143
	v_add_f32_e32 v129, 1.0, v129
	v_add_f32_e32 v132, 1.0, v132
	v_add_f32_e32 v133, 1.0, v133
	v_add_f32_e32 v140, 1.0, v140
	v_add_f32_e32 v141, 1.0, v141
	v_rcp_f32_e32 v128, v128
	v_rcp_f32_e32 v129, v129
	v_rcp_f32_e32 v132, v132
	v_rcp_f32_e32 v133, v133
	v_rcp_f32_e32 v136, v136
	v_rcp_f32_e32 v137, v137
	v_rcp_f32_e32 v140, v140
	v_rcp_f32_e32 v141, v141
	v_pk_mul_f32 v[128:129], v[128:129], v[130:131]
	v_pk_mul_f32 v[130:131], v[132:133], v[134:135]
	v_pk_mul_f32 v[132:133], v[136:137], v[138:139]
	v_pk_mul_f32 v[134:135], v[140:141], v[142:143]
	v_pk_mul_f32 v[70:71], v[70:71], v[130:131]
	v_pk_mul_f32 v[68:69], v[68:69], v[128:129]
	v_pk_mul_f32 v[66:67], v[66:67], v[134:135]
	v_pk_mul_f32 v[64:65], v[64:65], v[132:133]
	global_load_dwordx4 v[212:215], v[186:187], off offset:256
	global_load_dwordx4 v[216:219], v[158:159], off offset:256
	global_load_dwordx4 v[140:143], v[188:189], off
	global_load_dwordx4 v[132:135], v[188:189], off offset:256
	global_load_dwordx4 v[136:139], v[160:161], off
	global_load_dwordx4 v[128:131], v[160:161], off offset:256
	s_waitcnt vmcnt(7)
	v_lshlrev_b32_e32 v220, 16, v204
	v_and_b32_e32 v221, 0xffff0000, v204
	s_waitcnt vmcnt(6)
	v_lshlrev_b32_e32 v204, 16, v208
	v_mul_f32_e32 v204, 0xbfb8aa3b, v204
	v_exp_f32_e32 v204, v204
	v_lshlrev_b32_e32 v222, 16, v205
	v_and_b32_e32 v223, 0xffff0000, v205
	v_lshlrev_b32_e32 v224, 16, v206
	v_and_b32_e32 v225, 0xffff0000, v206
	v_and_b32_e32 v205, 0xffff0000, v208
	v_mul_f32_e32 v206, 0xbfb8aa3b, v220
	v_exp_f32_e32 v206, v206
	v_add_f32_e32 v204, 1.0, v204
	v_mul_f32_e32 v205, 0xbfb8aa3b, v205
	v_min_f32_e32 v208, 0x49800000, v204
	v_exp_f32_e32 v205, v205
	v_add_f32_e32 v206, 1.0, v206
	v_rcp_f32_e32 v204, v206
	v_mov_b32_e32 v206, v208
	v_mul_f32_e32 v208, 0xbfb8aa3b, v221
	v_add_f32_e32 v205, 1.0, v205
	v_lshlrev_b32_e32 v228, 16, v210
	v_and_b32_e32 v229, 0xffff0000, v210
	v_exp_f32_e32 v208, v208
	v_min_f32_e32 v210, 0x49800000, v205
	v_lshlrev_b32_e32 v226, 16, v207
	v_and_b32_e32 v227, 0xffff0000, v207
	v_lshlrev_b32_e32 v207, 16, v209
	v_add_f32_e32 v205, 1.0, v208
	v_mov_b32_e32 v208, v210
	v_mul_f32_e32 v210, 0xbfb8aa3b, v222
	v_mul_f32_e32 v207, 0xbfb8aa3b, v207
	v_lshlrev_b32_e32 v230, 16, v211
	v_and_b32_e32 v231, 0xffff0000, v211
	v_exp_f32_e32 v210, v210
	v_exp_f32_e32 v211, v207
	v_and_b32_e32 v209, 0xffff0000, v209
	v_mov_b32_e32 v207, v208
	v_add_f32_e32 v208, 1.0, v210
	v_add_f32_e32 v210, 1.0, v211
	v_mul_f32_e32 v211, 0xbfb8aa3b, v223
	v_mul_f32_e32 v209, 0xbfb8aa3b, v209
	v_exp_f32_e32 v211, v211
	v_exp_f32_e32 v209, v209
	v_mul_f32_e32 v221, 0xbfb8aa3b, v224
	v_exp_f32_e32 v221, v221
	v_add_f32_e32 v211, 1.0, v211
	v_add_f32_e32 v209, 1.0, v209
	v_min_f32_e32 v220, 0x49800000, v209
	v_rcp_f32_e32 v209, v211
	v_mul_f32_e32 v211, 0xbfb8aa3b, v228
	v_exp_f32_e32 v211, v211
	v_min_f32_e32 v210, 0x49800000, v210
	v_add_f32_e32 v211, 1.0, v211
	v_min_f32_e32 v222, 0x49800000, v211
	v_mov_b32_e32 v211, v220
	v_add_f32_e32 v220, 1.0, v221
	v_mov_b32_e32 v221, v222
	v_mul_f32_e32 v222, 0xbfb8aa3b, v225
	v_exp_f32_e32 v223, v222
	v_mul_f32_e32 v222, 0xbfb8aa3b, v229
	v_exp_f32_e32 v224, v222
	v_mov_b32_e32 v222, v221
	v_add_f32_e32 v221, 1.0, v223
	v_mul_f32_e32 v225, 0xbfb8aa3b, v230
	v_add_f32_e32 v223, 1.0, v224
	v_min_f32_e32 v223, 0x49800000, v223
	v_mul_f32_e32 v224, 0xbfb8aa3b, v226
	v_exp_f32_e32 v225, v225
	v_mul_f32_e32 v226, 0xbfb8aa3b, v231
	v_exp_f32_e32 v226, v226
	v_rcp_f32_e32 v205, v205
	v_rcp_f32_e32 v208, v208
	v_rcp_f32_e32 v220, v220
	v_rcp_f32_e32 v221, v221
	v_add_f32_e32 v225, 1.0, v225
	v_min_f32_e32 v225, 0x49800000, v225
	v_mul_f32_e32 v227, 0xbfb8aa3b, v227
	v_add_f32_e32 v226, 1.0, v226
	v_exp_f32_e32 v224, v224
	v_exp_f32_e32 v227, v227
	v_min_f32_e32 v228, 0x49800000, v226
	v_pk_mul_f32 v[204:205], v[204:205], v[206:207]
	v_pk_mul_f32 v[206:207], v[208:209], v[210:211]
	v_pk_mul_f32 v[208:209], v[220:221], v[222:223]
	v_pk_mul_f32 v[56:57], v[56:57], v[208:209]
	s_waitcnt vmcnt(4)
	v_and_b32_e32 v208, 0xffff0000, v216
	v_mul_f32_e32 v208, 0xbfb8aa3b, v208
	v_add_f32_e32 v224, 1.0, v224
	v_mov_b32_e32 v226, v225
	v_add_f32_e32 v225, 1.0, v227
	v_mov_b32_e32 v227, v228
	v_exp_f32_e32 v208, v208
	v_rcp_f32_e32 v224, v224
	v_rcp_f32_e32 v225, v225
	v_pk_mul_f32 v[60:61], v[60:61], v[204:205]
	v_lshlrev_b32_e32 v204, 16, v212
	v_and_b32_e32 v205, 0xffff0000, v212
	v_and_b32_e32 v212, 0xffff0000, v217
	v_mul_f32_e32 v212, 0xbfb8aa3b, v212
	v_pk_mul_f32 v[62:63], v[62:63], v[206:207]
	v_lshlrev_b32_e32 v207, 16, v213
	v_add_f32_e32 v208, 1.0, v208
	v_exp_f32_e32 v212, v212
	v_pk_mul_f32 v[210:211], v[224:225], v[226:227]
	v_min_f32_e32 v208, 0x49800000, v208
	v_mul_f32_e32 v207, 0xbfb8aa3b, v207
	v_pk_mul_f32 v[58:59], v[58:59], v[210:211]
	v_and_b32_e32 v209, 0xffff0000, v213
	v_lshlrev_b32_e32 v211, 16, v214
	v_and_b32_e32 v213, 0xffff0000, v214
	v_lshlrev_b32_e32 v220, 16, v215
	v_and_b32_e32 v221, 0xffff0000, v215
	v_lshlrev_b32_e32 v214, 16, v218
	v_and_b32_e32 v215, 0xffff0000, v218
	v_exp_f32_e32 v218, v207
	v_lshlrev_b32_e32 v210, 16, v217
	v_add_f32_e32 v212, 1.0, v212
	v_mul_f32_e32 v214, 0xbfb8aa3b, v214
	v_lshlrev_b32_e32 v206, 16, v216
	v_lshlrev_b32_e32 v216, 16, v219
	v_mul_f32_e32 v207, 0xbfb8aa3b, v210
	v_min_f32_e32 v212, 0x49800000, v212
	v_exp_f32_e32 v214, v214
	v_mul_f32_e32 v211, 0xbfb8aa3b, v211
	v_exp_f32_e32 v210, v207
	v_mov_b32_e32 v207, v208
	v_add_f32_e32 v208, 1.0, v218
	v_exp_f32_e32 v218, v211
	v_mul_f32_e32 v216, 0xbfb8aa3b, v216
	v_exp_f32_e32 v216, v216
	v_add_f32_e32 v211, 1.0, v214
	v_mul_f32_e32 v206, 0xbfb8aa3b, v206
	v_and_b32_e32 v217, 0xffff0000, v219
	v_min_f32_e32 v214, 0x49800000, v211
	v_mov_b32_e32 v211, v212
	v_add_f32_e32 v212, 1.0, v218
	v_mul_f32_e32 v218, 0xbfb8aa3b, v220
	v_exp_f32_e32 v206, v206
	v_mul_f32_e32 v215, 0xbfb8aa3b, v215
	v_exp_f32_e32 v218, v218
	v_add_f32_e32 v216, 1.0, v216
	v_mul_f32_e32 v217, 0xbfb8aa3b, v217
	v_exp_f32_e32 v215, v215
	v_min_f32_e32 v219, 0x49800000, v216
	v_exp_f32_e32 v217, v217
	v_mul_f32_e32 v204, 0xbfb8aa3b, v204
	v_add_f32_e32 v206, 1.0, v206
	v_mul_f32_e32 v205, 0xbfb8aa3b, v205
	v_add_f32_e32 v210, 1.0, v210
	v_mul_f32_e32 v209, 0xbfb8aa3b, v209
	v_add_f32_e32 v218, 1.0, v218
	v_exp_f32_e32 v204, v204
	v_min_f32_e32 v206, 0x49800000, v206
	v_exp_f32_e32 v205, v205
	v_min_f32_e32 v210, 0x49800000, v210
	v_exp_f32_e32 v209, v209
	v_mul_f32_e32 v213, 0xbfb8aa3b, v213
	v_add_f32_e32 v215, 1.0, v215
	v_rcp_f32_e32 v216, v218
	v_mov_b32_e32 v218, v219
	v_mul_f32_e32 v219, 0xbfb8aa3b, v221
	v_add_f32_e32 v217, 1.0, v217
	v_exp_f32_e32 v213, v213
	v_min_f32_e32 v215, 0x49800000, v215
	v_exp_f32_e32 v219, v219
	v_min_f32_e32 v220, 0x49800000, v217
	v_add_f32_e32 v204, 1.0, v204
	v_add_f32_e32 v205, 1.0, v205
	v_add_f32_e32 v209, 1.0, v209
	v_rcp_f32_e32 v204, v204
	v_rcp_f32_e32 v205, v205
	v_rcp_f32_e32 v208, v208
	v_rcp_f32_e32 v209, v209
	v_add_f32_e32 v213, 1.0, v213
	v_add_f32_e32 v217, 1.0, v219
	v_mov_b32_e32 v219, v220
	v_rcp_f32_e32 v212, v212
	v_rcp_f32_e32 v213, v213
	v_rcp_f32_e32 v217, v217
	v_pk_mul_f32 v[204:205], v[204:205], v[206:207]
	v_pk_mul_f32 v[206:207], v[208:209], v[210:211]
	v_pk_mul_f32 v[208:209], v[212:213], v[214:215]
	v_pk_mul_f32 v[210:211], v[216:217], v[218:219]
	v_pk_mul_f32 v[54:55], v[54:55], v[206:207]
	s_waitcnt vmcnt(3)
	v_lshlrev_b32_e32 v206, 16, v142
	v_and_b32_e32 v207, 0xffff0000, v142
	s_waitcnt vmcnt(1)
	v_lshlrev_b32_e32 v142, 16, v136
	v_pk_mul_f32 v[50:51], v[50:51], v[210:211]
	v_pk_mul_f32 v[48:49], v[48:49], v[208:209]
	v_lshlrev_b32_e32 v208, 16, v143
	v_and_b32_e32 v209, 0xffff0000, v143
	v_and_b32_e32 v143, 0xffff0000, v136
	v_lshlrev_b32_e32 v210, 16, v137
	v_and_b32_e32 v211, 0xffff0000, v137
	v_mul_f32_e32 v137, 0xbfb8aa3b, v142
	v_lshlrev_b32_e32 v212, 16, v138
	v_and_b32_e32 v213, 0xffff0000, v138
	v_exp_f32_e32 v137, v137
	v_mul_f32_e32 v138, 0xbfb8aa3b, v143
	v_exp_f32_e32 v138, v138
	v_pk_mul_f32 v[52:53], v[52:53], v[204:205]
	v_lshlrev_b32_e32 v204, 16, v140
	v_and_b32_e32 v140, 0xffff0000, v140
	v_add_f32_e32 v137, 1.0, v137
	v_mul_f32_e32 v136, 0xbfb8aa3b, v204
	v_lshlrev_b32_e32 v214, 16, v139
	v_and_b32_e32 v215, 0xffff0000, v139
	v_min_f32_e32 v137, 0x49800000, v137
	v_mul_f32_e32 v139, 0xbfb8aa3b, v140
	v_add_f32_e32 v138, 1.0, v138
	v_mul_f32_e32 v204, 0xbfb8aa3b, v212
	v_exp_f32_e32 v139, v139
	v_min_f32_e32 v140, 0x49800000, v138
	v_exp_f32_e32 v204, v204
	v_lshlrev_b32_e32 v205, 16, v141
	v_mov_b32_e32 v138, v137
	v_add_f32_e32 v137, 1.0, v139
	v_mov_b32_e32 v139, v140
	v_mul_f32_e32 v140, 0xbfb8aa3b, v205
	v_mul_f32_e32 v205, 0xbfb8aa3b, v206
	v_add_f32_e32 v204, 1.0, v204
	v_exp_f32_e32 v205, v205
	v_min_f32_e32 v206, 0x49800000, v204
	v_mul_f32_e32 v142, 0xbfb8aa3b, v210
	v_mul_f32_e32 v143, 0xbfb8aa3b, v211
	v_add_f32_e32 v204, 1.0, v205
	v_mov_b32_e32 v205, v206
	v_mul_f32_e32 v206, 0xbfb8aa3b, v207
	v_exp_f32_e32 v207, v206
	v_mul_f32_e32 v206, 0xbfb8aa3b, v213
	v_exp_f32_e32 v210, v206
	v_mov_b32_e32 v206, v205
	v_add_f32_e32 v205, 1.0, v207
	v_mul_f32_e32 v211, 0xbfb8aa3b, v215
	v_add_f32_e32 v207, 1.0, v210
	v_mul_f32_e32 v210, 0xbfb8aa3b, v214
	v_exp_f32_e32 v142, v142
	v_exp_f32_e32 v143, v143
	v_exp_f32_e32 v210, v210
	v_exp_f32_e32 v211, v211
	v_and_b32_e32 v141, 0xffff0000, v141
	v_add_f32_e32 v142, 1.0, v142
	v_mul_f32_e32 v141, 0xbfb8aa3b, v141
	v_add_f32_e32 v143, 1.0, v143
	v_mul_f32_e32 v208, 0xbfb8aa3b, v208
	v_add_f32_e32 v210, 1.0, v210
	v_mul_f32_e32 v209, 0xbfb8aa3b, v209
	v_add_f32_e32 v211, 1.0, v211
	v_exp_f32_e32 v136, v136
	v_exp_f32_e32 v140, v140
	v_min_f32_e32 v142, 0x49800000, v142
	v_exp_f32_e32 v141, v141
	v_min_f32_e32 v143, 0x49800000, v143
	v_min_f32_e32 v207, 0x49800000, v207
	v_exp_f32_e32 v208, v208
	v_min_f32_e32 v210, 0x49800000, v210
	v_exp_f32_e32 v209, v209
	v_min_f32_e32 v211, 0x49800000, v211
	v_add_f32_e32 v136, 1.0, v136
	v_add_f32_e32 v140, 1.0, v140
	v_add_f32_e32 v141, 1.0, v141
	v_add_f32_e32 v208, 1.0, v208
	v_add_f32_e32 v209, 1.0, v209
	v_rcp_f32_e32 v136, v136
	v_rcp_f32_e32 v137, v137
	v_rcp_f32_e32 v140, v140
	v_rcp_f32_e32 v141, v141
	v_rcp_f32_e32 v204, v204
	v_rcp_f32_e32 v205, v205
	v_rcp_f32_e32 v208, v208
	v_rcp_f32_e32 v209, v209
	v_pk_mul_f32 v[136:137], v[136:137], v[138:139]
	v_pk_mul_f32 v[138:139], v[140:141], v[142:143]
	v_pk_mul_f32 v[140:141], v[204:205], v[206:207]
	v_pk_mul_f32 v[142:143], v[208:209], v[210:211]
	global_load_dwordx4 v[204:207], v[190:191], off
	global_load_dwordx4 v[208:211], v[162:163], off
	v_pk_mul_f32 v[46:47], v[46:47], v[138:139]
	v_lshlrev_b32_e32 v138, 16, v134
	v_and_b32_e32 v139, 0xffff0000, v134
	s_waitcnt vmcnt(2)
	v_lshlrev_b32_e32 v134, 16, v128
	v_pk_mul_f32 v[40:41], v[40:41], v[140:141]
	v_lshlrev_b32_e32 v140, 16, v135
	v_and_b32_e32 v141, 0xffff0000, v135
	v_and_b32_e32 v135, 0xffff0000, v128
	v_mul_f32_e32 v128, 0xbfb8aa3b, v134
	v_exp_f32_e32 v128, v128
	v_pk_mul_f32 v[44:45], v[44:45], v[136:137]
	v_lshlrev_b32_e32 v136, 16, v132
	v_pk_mul_f32 v[42:43], v[42:43], v[142:143]
	v_lshlrev_b32_e32 v142, 16, v129
	v_and_b32_e32 v143, 0xffff0000, v129
	v_lshlrev_b32_e32 v212, 16, v130
	v_mul_f32_e32 v129, 0xbfb8aa3b, v136
	v_add_f32_e32 v128, 1.0, v128
	v_and_b32_e32 v213, 0xffff0000, v130
	v_exp_f32_e32 v129, v129
	v_min_f32_e32 v130, 0x49800000, v128
	v_mul_f32_e32 v136, 0xbfb8aa3b, v212
	v_exp_f32_e32 v136, v136
	v_and_b32_e32 v132, 0xffff0000, v132
	v_lshlrev_b32_e32 v137, 16, v133
	v_add_f32_e32 v128, 1.0, v129
	v_mov_b32_e32 v129, v130
	v_mul_f32_e32 v130, 0xbfb8aa3b, v135
	v_lshlrev_b32_e32 v214, 16, v131
	v_and_b32_e32 v215, 0xffff0000, v131
	v_exp_f32_e32 v131, v130
	v_mov_b32_e32 v130, v129
	v_mul_f32_e32 v129, 0xbfb8aa3b, v132
	v_mul_f32_e32 v132, 0xbfb8aa3b, v137
	v_mul_f32_e32 v137, 0xbfb8aa3b, v138
	v_add_f32_e32 v136, 1.0, v136
	v_exp_f32_e32 v137, v137
	v_min_f32_e32 v138, 0x49800000, v136
	v_mul_f32_e32 v134, 0xbfb8aa3b, v142
	v_mul_f32_e32 v135, 0xbfb8aa3b, v143
	v_add_f32_e32 v136, 1.0, v137
	v_mov_b32_e32 v137, v138
	v_mul_f32_e32 v138, 0xbfb8aa3b, v139
	v_exp_f32_e32 v139, v138
	v_mul_f32_e32 v138, 0xbfb8aa3b, v213
	v_exp_f32_e32 v142, v138
	v_mov_b32_e32 v138, v137
	v_add_f32_e32 v137, 1.0, v139
	v_mul_f32_e32 v143, 0xbfb8aa3b, v215
	v_add_f32_e32 v139, 1.0, v142
	v_mul_f32_e32 v142, 0xbfb8aa3b, v214
	v_exp_f32_e32 v134, v134
	v_exp_f32_e32 v135, v135
	v_exp_f32_e32 v142, v142
	v_exp_f32_e32 v143, v143
	v_and_b32_e32 v133, 0xffff0000, v133
	v_add_f32_e32 v131, 1.0, v131
	v_add_f32_e32 v134, 1.0, v134
	v_mul_f32_e32 v133, 0xbfb8aa3b, v133
	v_add_f32_e32 v135, 1.0, v135
	v_mul_f32_e32 v140, 0xbfb8aa3b, v140
	v_add_f32_e32 v142, 1.0, v142
	v_mul_f32_e32 v141, 0xbfb8aa3b, v141
	v_add_f32_e32 v143, 1.0, v143
	v_exp_f32_e32 v129, v129
	v_min_f32_e32 v131, 0x49800000, v131
	v_exp_f32_e32 v132, v132
	v_min_f32_e32 v134, 0x49800000, v134
	v_exp_f32_e32 v133, v133
	v_min_f32_e32 v135, 0x49800000, v135
	v_min_f32_e32 v139, 0x49800000, v139
	v_exp_f32_e32 v140, v140
	v_min_f32_e32 v142, 0x49800000, v142
	v_exp_f32_e32 v141, v141
	v_min_f32_e32 v143, 0x49800000, v143
	v_add_f32_e32 v129, 1.0, v129
	v_add_f32_e32 v132, 1.0, v132
	v_add_f32_e32 v133, 1.0, v133
	v_add_f32_e32 v140, 1.0, v140
	v_add_f32_e32 v141, 1.0, v141
	v_rcp_f32_e32 v128, v128
	v_rcp_f32_e32 v129, v129
	v_rcp_f32_e32 v132, v132
	v_rcp_f32_e32 v133, v133
	v_rcp_f32_e32 v136, v136
	v_rcp_f32_e32 v137, v137
	v_rcp_f32_e32 v140, v140
	v_rcp_f32_e32 v141, v141
	v_pk_mul_f32 v[128:129], v[128:129], v[130:131]
	v_pk_mul_f32 v[130:131], v[132:133], v[134:135]
	v_pk_mul_f32 v[132:133], v[136:137], v[138:139]
	v_pk_mul_f32 v[134:135], v[140:141], v[142:143]
	v_pk_mul_f32 v[38:39], v[38:39], v[130:131]
	v_pk_mul_f32 v[36:37], v[36:37], v[128:129]
	v_pk_mul_f32 v[34:35], v[34:35], v[134:135]
	v_pk_mul_f32 v[32:33], v[32:33], v[132:133]
	global_load_dwordx4 v[212:215], v[190:191], off offset:256
	global_load_dwordx4 v[216:219], v[162:163], off offset:256
	global_load_dwordx4 v[140:143], v[192:193], off
	global_load_dwordx4 v[132:135], v[192:193], off offset:256
	global_load_dwordx4 v[136:139], v[164:165], off
	global_load_dwordx4 v[128:131], v[164:165], off offset:256
	s_waitcnt vmcnt(7)
	v_lshlrev_b32_e32 v220, 16, v204
	v_and_b32_e32 v221, 0xffff0000, v204
	s_waitcnt vmcnt(6)
	v_lshlrev_b32_e32 v204, 16, v208
	v_mul_f32_e32 v204, 0xbfb8aa3b, v204
	v_exp_f32_e32 v204, v204
	v_lshlrev_b32_e32 v222, 16, v205
	v_and_b32_e32 v223, 0xffff0000, v205
	v_lshlrev_b32_e32 v224, 16, v206
	v_and_b32_e32 v225, 0xffff0000, v206
	v_and_b32_e32 v205, 0xffff0000, v208
	v_mul_f32_e32 v206, 0xbfb8aa3b, v220
	v_exp_f32_e32 v206, v206
	v_add_f32_e32 v204, 1.0, v204
	v_mul_f32_e32 v205, 0xbfb8aa3b, v205
	v_min_f32_e32 v208, 0x49800000, v204
	v_exp_f32_e32 v205, v205
	v_add_f32_e32 v206, 1.0, v206
	v_rcp_f32_e32 v204, v206
	v_mov_b32_e32 v206, v208
	v_mul_f32_e32 v208, 0xbfb8aa3b, v221
	v_add_f32_e32 v205, 1.0, v205
	v_lshlrev_b32_e32 v228, 16, v210
	v_and_b32_e32 v229, 0xffff0000, v210
	v_exp_f32_e32 v208, v208
	v_min_f32_e32 v210, 0x49800000, v205
	v_lshlrev_b32_e32 v226, 16, v207
	v_and_b32_e32 v227, 0xffff0000, v207
	v_lshlrev_b32_e32 v207, 16, v209
	v_add_f32_e32 v205, 1.0, v208
	v_mov_b32_e32 v208, v210
	v_mul_f32_e32 v210, 0xbfb8aa3b, v222
	v_mul_f32_e32 v207, 0xbfb8aa3b, v207
	v_lshlrev_b32_e32 v230, 16, v211
	v_and_b32_e32 v231, 0xffff0000, v211
	v_exp_f32_e32 v210, v210
	v_exp_f32_e32 v211, v207
	v_and_b32_e32 v209, 0xffff0000, v209
	v_mov_b32_e32 v207, v208
	v_add_f32_e32 v208, 1.0, v210
	v_add_f32_e32 v210, 1.0, v211
	v_mul_f32_e32 v211, 0xbfb8aa3b, v223
	v_mul_f32_e32 v209, 0xbfb8aa3b, v209
	v_exp_f32_e32 v211, v211
	v_exp_f32_e32 v209, v209
	v_mul_f32_e32 v221, 0xbfb8aa3b, v224
	v_exp_f32_e32 v221, v221
	v_add_f32_e32 v211, 1.0, v211
	v_add_f32_e32 v209, 1.0, v209
	v_min_f32_e32 v220, 0x49800000, v209
	v_rcp_f32_e32 v209, v211
	v_mul_f32_e32 v211, 0xbfb8aa3b, v228
	v_exp_f32_e32 v211, v211
	v_min_f32_e32 v210, 0x49800000, v210
	v_add_f32_e32 v211, 1.0, v211
	v_min_f32_e32 v222, 0x49800000, v211
	v_mov_b32_e32 v211, v220
	v_add_f32_e32 v220, 1.0, v221
	v_mov_b32_e32 v221, v222
	v_mul_f32_e32 v222, 0xbfb8aa3b, v225
	v_exp_f32_e32 v223, v222
	v_mul_f32_e32 v222, 0xbfb8aa3b, v229
	v_exp_f32_e32 v224, v222
	v_mov_b32_e32 v222, v221
	v_add_f32_e32 v221, 1.0, v223
	v_mul_f32_e32 v225, 0xbfb8aa3b, v230
	v_add_f32_e32 v223, 1.0, v224
	v_min_f32_e32 v223, 0x49800000, v223
	v_mul_f32_e32 v224, 0xbfb8aa3b, v226
	v_exp_f32_e32 v225, v225
	v_mul_f32_e32 v226, 0xbfb8aa3b, v231
	v_exp_f32_e32 v226, v226
	v_rcp_f32_e32 v205, v205
	v_rcp_f32_e32 v208, v208
	v_rcp_f32_e32 v220, v220
	v_rcp_f32_e32 v221, v221
	v_add_f32_e32 v225, 1.0, v225
	v_min_f32_e32 v225, 0x49800000, v225
	v_mul_f32_e32 v227, 0xbfb8aa3b, v227
	v_add_f32_e32 v226, 1.0, v226
	v_exp_f32_e32 v224, v224
	v_exp_f32_e32 v227, v227
	v_min_f32_e32 v228, 0x49800000, v226
	v_pk_mul_f32 v[204:205], v[204:205], v[206:207]
	v_pk_mul_f32 v[206:207], v[208:209], v[210:211]
	v_pk_mul_f32 v[208:209], v[220:221], v[222:223]
	v_pk_mul_f32 v[24:25], v[24:25], v[208:209]
	s_waitcnt vmcnt(4)
	v_and_b32_e32 v208, 0xffff0000, v216
	v_mul_f32_e32 v208, 0xbfb8aa3b, v208
	v_add_f32_e32 v224, 1.0, v224
	v_mov_b32_e32 v226, v225
	v_add_f32_e32 v225, 1.0, v227
	v_mov_b32_e32 v227, v228
	v_exp_f32_e32 v208, v208
	v_rcp_f32_e32 v224, v224
	v_rcp_f32_e32 v225, v225
	v_pk_mul_f32 v[28:29], v[28:29], v[204:205]
	v_lshlrev_b32_e32 v204, 16, v212
	v_and_b32_e32 v205, 0xffff0000, v212
	v_and_b32_e32 v212, 0xffff0000, v217
	v_mul_f32_e32 v212, 0xbfb8aa3b, v212
	v_pk_mul_f32 v[30:31], v[30:31], v[206:207]
	v_lshlrev_b32_e32 v207, 16, v213
	v_add_f32_e32 v208, 1.0, v208
	v_exp_f32_e32 v212, v212
	v_pk_mul_f32 v[210:211], v[224:225], v[226:227]
	v_min_f32_e32 v208, 0x49800000, v208
	v_mul_f32_e32 v207, 0xbfb8aa3b, v207
	v_pk_mul_f32 v[26:27], v[26:27], v[210:211]
	v_and_b32_e32 v209, 0xffff0000, v213
	v_lshlrev_b32_e32 v211, 16, v214
	v_and_b32_e32 v213, 0xffff0000, v214
	v_lshlrev_b32_e32 v220, 16, v215
	v_and_b32_e32 v221, 0xffff0000, v215
	v_lshlrev_b32_e32 v214, 16, v218
	v_and_b32_e32 v215, 0xffff0000, v218
	v_exp_f32_e32 v218, v207
	v_lshlrev_b32_e32 v210, 16, v217
	v_add_f32_e32 v212, 1.0, v212
	v_mul_f32_e32 v214, 0xbfb8aa3b, v214
	v_lshlrev_b32_e32 v206, 16, v216
	v_lshlrev_b32_e32 v216, 16, v219
	v_mul_f32_e32 v207, 0xbfb8aa3b, v210
	v_min_f32_e32 v212, 0x49800000, v212
	v_exp_f32_e32 v214, v214
	v_mul_f32_e32 v211, 0xbfb8aa3b, v211
	v_exp_f32_e32 v210, v207
	v_mov_b32_e32 v207, v208
	v_add_f32_e32 v208, 1.0, v218
	v_exp_f32_e32 v218, v211
	v_mul_f32_e32 v216, 0xbfb8aa3b, v216
	v_exp_f32_e32 v216, v216
	v_add_f32_e32 v211, 1.0, v214
	v_mul_f32_e32 v206, 0xbfb8aa3b, v206
	v_and_b32_e32 v217, 0xffff0000, v219
	v_min_f32_e32 v214, 0x49800000, v211
	v_mov_b32_e32 v211, v212
	v_add_f32_e32 v212, 1.0, v218
	v_mul_f32_e32 v218, 0xbfb8aa3b, v220
	v_exp_f32_e32 v206, v206
	v_mul_f32_e32 v215, 0xbfb8aa3b, v215
	v_exp_f32_e32 v218, v218
	v_add_f32_e32 v216, 1.0, v216
	v_mul_f32_e32 v217, 0xbfb8aa3b, v217
	v_exp_f32_e32 v215, v215
	v_min_f32_e32 v219, 0x49800000, v216
	v_exp_f32_e32 v217, v217
	v_mul_f32_e32 v204, 0xbfb8aa3b, v204
	v_add_f32_e32 v206, 1.0, v206
	v_mul_f32_e32 v205, 0xbfb8aa3b, v205
	v_add_f32_e32 v210, 1.0, v210
	v_mul_f32_e32 v209, 0xbfb8aa3b, v209
	v_add_f32_e32 v218, 1.0, v218
	v_exp_f32_e32 v204, v204
	v_min_f32_e32 v206, 0x49800000, v206
	v_exp_f32_e32 v205, v205
	v_min_f32_e32 v210, 0x49800000, v210
	v_exp_f32_e32 v209, v209
	v_mul_f32_e32 v213, 0xbfb8aa3b, v213
	v_add_f32_e32 v215, 1.0, v215
	v_rcp_f32_e32 v216, v218
	v_mov_b32_e32 v218, v219
	v_mul_f32_e32 v219, 0xbfb8aa3b, v221
	v_add_f32_e32 v217, 1.0, v217
	v_exp_f32_e32 v213, v213
	v_min_f32_e32 v215, 0x49800000, v215
	v_exp_f32_e32 v219, v219
	v_min_f32_e32 v220, 0x49800000, v217
	v_add_f32_e32 v204, 1.0, v204
	v_add_f32_e32 v205, 1.0, v205
	v_add_f32_e32 v209, 1.0, v209
	v_rcp_f32_e32 v204, v204
	v_rcp_f32_e32 v205, v205
	v_rcp_f32_e32 v208, v208
	v_rcp_f32_e32 v209, v209
	v_add_f32_e32 v213, 1.0, v213
	v_add_f32_e32 v217, 1.0, v219
	v_mov_b32_e32 v219, v220
	v_rcp_f32_e32 v212, v212
	v_rcp_f32_e32 v213, v213
	v_rcp_f32_e32 v217, v217
	v_pk_mul_f32 v[204:205], v[204:205], v[206:207]
	v_pk_mul_f32 v[206:207], v[208:209], v[210:211]
	v_pk_mul_f32 v[208:209], v[212:213], v[214:215]
	v_pk_mul_f32 v[210:211], v[216:217], v[218:219]
	v_pk_mul_f32 v[22:23], v[22:23], v[206:207]
	s_waitcnt vmcnt(3)
	v_lshlrev_b32_e32 v206, 16, v142
	v_and_b32_e32 v207, 0xffff0000, v142
	s_waitcnt vmcnt(1)
	v_lshlrev_b32_e32 v142, 16, v136
	v_pk_mul_f32 v[18:19], v[18:19], v[210:211]
	v_pk_mul_f32 v[16:17], v[16:17], v[208:209]
	v_lshlrev_b32_e32 v208, 16, v143
	v_and_b32_e32 v209, 0xffff0000, v143
	v_and_b32_e32 v143, 0xffff0000, v136
	v_lshlrev_b32_e32 v210, 16, v137
	v_and_b32_e32 v211, 0xffff0000, v137
	v_mul_f32_e32 v137, 0xbfb8aa3b, v142
	v_lshlrev_b32_e32 v212, 16, v138
	v_and_b32_e32 v213, 0xffff0000, v138
	v_exp_f32_e32 v137, v137
	v_mul_f32_e32 v138, 0xbfb8aa3b, v143
	v_exp_f32_e32 v138, v138
	v_pk_mul_f32 v[20:21], v[20:21], v[204:205]
	v_lshlrev_b32_e32 v204, 16, v140
	v_and_b32_e32 v140, 0xffff0000, v140
	v_add_f32_e32 v137, 1.0, v137
	v_mul_f32_e32 v136, 0xbfb8aa3b, v204
	v_lshlrev_b32_e32 v214, 16, v139
	v_and_b32_e32 v215, 0xffff0000, v139
	v_min_f32_e32 v137, 0x49800000, v137
	v_mul_f32_e32 v139, 0xbfb8aa3b, v140
	v_add_f32_e32 v138, 1.0, v138
	v_mul_f32_e32 v204, 0xbfb8aa3b, v212
	v_exp_f32_e32 v139, v139
	v_min_f32_e32 v140, 0x49800000, v138
	v_exp_f32_e32 v204, v204
	v_lshlrev_b32_e32 v205, 16, v141
	v_mov_b32_e32 v138, v137
	v_add_f32_e32 v137, 1.0, v139
	v_mov_b32_e32 v139, v140
	v_mul_f32_e32 v140, 0xbfb8aa3b, v205
	v_mul_f32_e32 v205, 0xbfb8aa3b, v206
	v_add_f32_e32 v204, 1.0, v204
	v_exp_f32_e32 v205, v205
	v_min_f32_e32 v206, 0x49800000, v204
	v_mul_f32_e32 v142, 0xbfb8aa3b, v210
	v_mul_f32_e32 v143, 0xbfb8aa3b, v211
	v_add_f32_e32 v204, 1.0, v205
	v_mov_b32_e32 v205, v206
	v_mul_f32_e32 v206, 0xbfb8aa3b, v207
	v_exp_f32_e32 v207, v206
	v_mul_f32_e32 v206, 0xbfb8aa3b, v213
	v_exp_f32_e32 v210, v206
	v_exp_f32_e32 v142, v142
	v_exp_f32_e32 v143, v143
	v_mov_b32_e32 v206, v205
	v_add_f32_e32 v205, 1.0, v207
	v_add_f32_e32 v207, 1.0, v210
	v_mul_f32_e32 v210, 0xbfb8aa3b, v214
	v_mul_f32_e32 v211, 0xbfb8aa3b, v215
	v_exp_f32_e32 v210, v210
	v_exp_f32_e32 v211, v211
	v_and_b32_e32 v141, 0xffff0000, v141
	v_add_f32_e32 v142, 1.0, v142
	v_mul_f32_e32 v141, 0xbfb8aa3b, v141
	v_add_f32_e32 v143, 1.0, v143
	v_exp_f32_e32 v136, v136
	v_exp_f32_e32 v140, v140
	v_min_f32_e32 v142, 0x49800000, v142
	v_exp_f32_e32 v141, v141
	v_min_f32_e32 v143, 0x49800000, v143
	v_mul_f32_e32 v208, 0xbfb8aa3b, v208
	v_add_f32_e32 v210, 1.0, v210
	v_mul_f32_e32 v209, 0xbfb8aa3b, v209
	v_add_f32_e32 v211, 1.0, v211
	v_min_f32_e32 v207, 0x49800000, v207
	v_exp_f32_e32 v208, v208
	v_min_f32_e32 v210, 0x49800000, v210
	v_exp_f32_e32 v209, v209
	v_min_f32_e32 v211, 0x49800000, v211
	v_add_f32_e32 v136, 1.0, v136
	v_add_f32_e32 v140, 1.0, v140
	v_add_f32_e32 v141, 1.0, v141
	v_rcp_f32_e32 v136, v136
	v_rcp_f32_e32 v137, v137
	v_rcp_f32_e32 v140, v140
	v_rcp_f32_e32 v141, v141
	v_add_f32_e32 v208, 1.0, v208
	v_add_f32_e32 v209, 1.0, v209
	v_rcp_f32_e32 v204, v204
	v_rcp_f32_e32 v205, v205
	v_rcp_f32_e32 v208, v208
	v_rcp_f32_e32 v209, v209
	v_pk_mul_f32 v[136:137], v[136:137], v[138:139]
	v_pk_mul_f32 v[138:139], v[140:141], v[142:143]
	v_pk_mul_f32 v[140:141], v[204:205], v[206:207]
	v_pk_mul_f32 v[142:143], v[208:209], v[210:211]
	v_pk_mul_f32 v[14:15], v[14:15], v[138:139]
	v_lshlrev_b32_e32 v138, 16, v134
	v_and_b32_e32 v139, 0xffff0000, v134
	s_waitcnt vmcnt(0)
	v_lshlrev_b32_e32 v134, 16, v128
	v_pk_mul_f32 v[10:11], v[10:11], v[142:143]
	v_pk_mul_f32 v[8:9], v[8:9], v[140:141]
	v_lshlrev_b32_e32 v140, 16, v135
	v_and_b32_e32 v141, 0xffff0000, v135
	v_and_b32_e32 v135, 0xffff0000, v128
	v_lshlrev_b32_e32 v142, 16, v129
	v_and_b32_e32 v143, 0xffff0000, v129
	v_mul_f32_e32 v129, 0xbfb8aa3b, v134
	v_lshlrev_b32_e32 v204, 16, v130
	v_and_b32_e32 v205, 0xffff0000, v130
	v_exp_f32_e32 v129, v129
	v_mul_f32_e32 v130, 0xbfb8aa3b, v135
	v_exp_f32_e32 v130, v130
	v_pk_mul_f32 v[12:13], v[12:13], v[136:137]
	v_lshlrev_b32_e32 v136, 16, v132
	v_and_b32_e32 v132, 0xffff0000, v132
	v_add_f32_e32 v129, 1.0, v129
	v_mul_f32_e32 v128, 0xbfb8aa3b, v136
	v_lshlrev_b32_e32 v206, 16, v131
	v_and_b32_e32 v207, 0xffff0000, v131
	v_min_f32_e32 v129, 0x49800000, v129
	v_mul_f32_e32 v131, 0xbfb8aa3b, v132
	v_add_f32_e32 v130, 1.0, v130
	v_mul_f32_e32 v136, 0xbfb8aa3b, v204
	v_exp_f32_e32 v131, v131
	v_min_f32_e32 v132, 0x49800000, v130
	v_exp_f32_e32 v136, v136
	v_lshlrev_b32_e32 v137, 16, v133
	v_mov_b32_e32 v130, v129
	v_add_f32_e32 v129, 1.0, v131
	v_mov_b32_e32 v131, v132
	v_mul_f32_e32 v132, 0xbfb8aa3b, v137
	v_mul_f32_e32 v137, 0xbfb8aa3b, v138
	v_add_f32_e32 v136, 1.0, v136
	v_exp_f32_e32 v137, v137
	v_min_f32_e32 v138, 0x49800000, v136
	v_mul_f32_e32 v134, 0xbfb8aa3b, v142
	v_mul_f32_e32 v135, 0xbfb8aa3b, v143
	v_add_f32_e32 v136, 1.0, v137
	v_mov_b32_e32 v137, v138
	v_mul_f32_e32 v138, 0xbfb8aa3b, v139
	v_exp_f32_e32 v139, v138
	v_mul_f32_e32 v138, 0xbfb8aa3b, v205
	v_exp_f32_e32 v142, v138
	v_mov_b32_e32 v138, v137
	v_add_f32_e32 v137, 1.0, v139
	v_mul_f32_e32 v143, 0xbfb8aa3b, v207
	v_add_f32_e32 v139, 1.0, v142
	v_mul_f32_e32 v142, 0xbfb8aa3b, v206
	v_exp_f32_e32 v134, v134
	v_exp_f32_e32 v135, v135
	v_exp_f32_e32 v142, v142
	v_exp_f32_e32 v143, v143
	v_and_b32_e32 v133, 0xffff0000, v133
	v_add_f32_e32 v134, 1.0, v134
	v_mul_f32_e32 v133, 0xbfb8aa3b, v133
	v_add_f32_e32 v135, 1.0, v135
	v_mul_f32_e32 v140, 0xbfb8aa3b, v140
	v_add_f32_e32 v142, 1.0, v142
	v_mul_f32_e32 v141, 0xbfb8aa3b, v141
	v_add_f32_e32 v143, 1.0, v143
	v_exp_f32_e32 v128, v128
	v_exp_f32_e32 v132, v132
	v_min_f32_e32 v134, 0x49800000, v134
	v_exp_f32_e32 v133, v133
	v_min_f32_e32 v135, 0x49800000, v135
	v_min_f32_e32 v139, 0x49800000, v139
	v_exp_f32_e32 v140, v140
	v_min_f32_e32 v142, 0x49800000, v142
	v_exp_f32_e32 v141, v141
	v_min_f32_e32 v143, 0x49800000, v143
	v_add_f32_e32 v128, 1.0, v128
	v_add_f32_e32 v132, 1.0, v132
	v_add_f32_e32 v133, 1.0, v133
	v_add_f32_e32 v140, 1.0, v140
	v_add_f32_e32 v141, 1.0, v141
	v_rcp_f32_e32 v128, v128
	v_rcp_f32_e32 v129, v129
	v_rcp_f32_e32 v132, v132
	v_rcp_f32_e32 v133, v133
	v_rcp_f32_e32 v136, v136
	v_rcp_f32_e32 v137, v137
	v_rcp_f32_e32 v140, v140
	v_rcp_f32_e32 v141, v141
	v_pk_mul_f32 v[128:129], v[128:129], v[130:131]
	v_pk_mul_f32 v[130:131], v[132:133], v[134:135]
	v_pk_mul_f32 v[132:133], v[136:137], v[138:139]
	v_pk_mul_f32 v[134:135], v[140:141], v[142:143]
	v_pk_mul_f32 v[2:3], v[2:3], v[130:131]
	v_pk_mul_f32 v[0:1], v[0:1], v[128:129]
	v_pk_mul_f32 v[6:7], v[6:7], v[134:135]
	v_pk_mul_f32 v[4:5], v[4:5], v[132:133]

.LBB0_1160:
	v_lshl_or_b32 v148, s65, 8, v161
	v_ashrrev_i32_e32 v149, 31, v148
	s_nop 15
	s_nop 15
	v_add_u32_e32 v144, s39, v160
	v_cmp_gt_i32_e32 vcc, s38, v160
	v_ashrrev_i32_e32 v150, 1, v148
	v_cndmask_b32_e32 v144, -1, v144, vcc
	v_cmp_lt_i32_e32 vcc, -1, v144
	v_ashrrev_i32_e32 v151, 31, v150
	s_and_saveexec_b64 s[10:11], vcc
	s_cbranch_execz .LBB0_1162
	v_pk_fma_f32 v[124:125], v[124:125], s[20:21], v[232:233] op_sel_hi:[1,0,1]
	v_lshlrev_b64 v[176:177], 11, v[144:145]
	v_min_f32_e32 v124, 0x40e00000, v124
	v_mul_f32_e32 v144, 0xc01d265f, v124
	v_exp_f32_e32 v144, v144
	v_pk_fma_f32 v[126:127], v[126:127], s[20:21], v[234:235] op_sel_hi:[1,0,1]
	v_pk_fma_f32 v[120:121], v[120:121], s[20:21], v[236:237] op_sel_hi:[1,0,1]
	v_min_f32_e32 v126, 0x40e00000, v126
	v_add_f32_e32 v144, 1.0, v144
	v_mul_f32_e32 v149, 0xc01d265f, v126
	v_rcp_f32_e32 v144, v144
	v_exp_f32_e32 v149, v149
	v_med3_f32 v125, v125, s61, v172
	v_mul_f32_e32 v124, v124, v144
	v_min_f32_e32 v120, 0x40e00000, v120
	v_add_f32_e32 v144, 1.0, v149
	v_fma_f32 v124, v125, v124, v124
	v_med3_f32 v125, v127, s61, v172
	v_mul_f32_e32 v127, 0xc01d265f, v120
	v_rcp_f32_e32 v144, v144
	v_exp_f32_e32 v127, v127
	v_pk_fma_f32 v[122:123], v[122:123], s[20:21], v[238:239] op_sel_hi:[1,0,1]
	v_mul_f32_e32 v126, v126, v144
	v_min_f32_e32 v122, 0x40e00000, v122
	v_fma_f32 v125, v125, v126, v126
	v_add_f32_e32 v126, 1.0, v127
	v_mul_f32_e32 v127, 0xc01d265f, v122
	v_rcp_f32_e32 v126, v126
	v_exp_f32_e32 v127, v127
	v_med3_f32 v121, v121, s61, v172
	v_mul_f32_e32 v120, v120, v126
	v_fma_f32 v120, v121, v120, v120
	v_add_f32_e32 v121, 1.0, v127
	v_rcp_f32_e32 v121, v121
	v_cvt_pk_fp8_f32 v200, v124, v125
	v_med3_f32 v123, v123, s61, v172
	v_mul_f32_e32 v121, v122, v121
	v_pk_fma_f32 v[116:117], v[116:117], s[20:21], v[240:241] op_sel_hi:[1,0,1]
	v_fma_f32 v121, v123, v121, v121
	v_min_f32_e32 v116, 0x40e00000, v116
	v_cvt_pk_fp8_f32 v200, v120, v121 op_sel:[0,0,1]
	v_mul_f32_e32 v120, 0xc01d265f, v116
	v_exp_f32_e32 v122, v120
	v_pk_fma_f32 v[118:119], v[118:119], s[20:21], v[242:243] op_sel_hi:[1,0,1]
	v_pk_fma_f32 v[112:113], v[112:113], s[20:21], v[244:245] op_sel_hi:[1,0,1]
	v_min_f32_e32 v118, 0x40e00000, v118
	v_add_f32_e32 v122, 1.0, v122
	v_mul_f32_e32 v123, 0xc01d265f, v118
	v_rcp_f32_e32 v122, v122
	v_exp_f32_e32 v123, v123
	v_med3_f32 v117, v117, s61, v172
	v_mul_f32_e32 v116, v116, v122
	v_min_f32_e32 v112, 0x40e00000, v112
	v_add_f32_e32 v122, 1.0, v123
	v_fma_f32 v116, v117, v116, v116
	v_med3_f32 v117, v119, s61, v172
	v_mul_f32_e32 v119, 0xc01d265f, v112
	v_rcp_f32_e32 v122, v122
	v_exp_f32_e32 v119, v119
	v_pk_fma_f32 v[114:115], v[114:115], s[20:21], v[246:247] op_sel_hi:[1,0,1]
	v_mul_f32_e32 v118, v118, v122
	v_min_f32_e32 v114, 0x40e00000, v114
	v_fma_f32 v117, v117, v118, v118
	v_add_f32_e32 v118, 1.0, v119
	v_mul_f32_e32 v119, 0xc01d265f, v114
	v_rcp_f32_e32 v118, v118
	v_exp_f32_e32 v119, v119
	v_med3_f32 v113, v113, s61, v172
	v_mul_f32_e32 v112, v112, v118
	v_fma_f32 v112, v113, v112, v112
	v_add_f32_e32 v113, 1.0, v119
	v_rcp_f32_e32 v113, v113
	v_cvt_pk_fp8_f32 v201, v116, v117
	v_med3_f32 v115, v115, s61, v172
	v_mul_f32_e32 v113, v114, v113
	v_fma_f32 v113, v115, v113, v113
	v_cvt_pk_fp8_f32 v201, v112, v113 op_sel:[0,0,1]
	v_lshl_add_u64 v[176:177], s[16:17], 0, v[176:177]
	v_lshl_add_u64 v[120:121], v[176:177], 0, v[150:151]
	global_store_dwordx2 v[120:121], v[200:201], off
.LBB0_1162:
	s_or_b64 exec, exec, s[10:11]
	v_add_u32_e32 v112, s39, v162
	v_cmp_gt_i32_e32 vcc, s38, v162
	s_nop 1
	v_cndmask_b32_e32 v144, -1, v112, vcc
	v_cmp_lt_i32_e32 vcc, -1, v144
	s_and_saveexec_b64 s[10:11], vcc
	s_cbranch_execz .LBB0_1164
	v_pk_fma_f32 v[108:109], v[108:109], s[20:21], v[232:233] op_sel_hi:[1,0,1]
	v_pk_fma_f32 v[110:111], v[110:111], s[20:21], v[234:235] op_sel_hi:[1,0,1]
	v_min_f32_e32 v108, 0x40e00000, v108
	v_mul_f32_e32 v114, 0xc01d265f, v108
	v_exp_f32_e32 v114, v114
	v_min_f32_e32 v110, 0x40e00000, v110
	v_mul_f32_e32 v115, 0xc01d265f, v110
	v_add_f32_e32 v114, 1.0, v114
	v_rcp_f32_e32 v114, v114
	v_exp_f32_e32 v115, v115
	v_pk_fma_f32 v[104:105], v[104:105], s[20:21], v[236:237] op_sel_hi:[1,0,1]
	v_med3_f32 v109, v109, s61, v172
	v_mul_f32_e32 v108, v108, v114
	v_min_f32_e32 v104, 0x40e00000, v104
	v_add_f32_e32 v114, 1.0, v115
	v_fma_f32 v108, v109, v108, v108
	v_med3_f32 v109, v111, s61, v172
	v_mul_f32_e32 v111, 0xc01d265f, v104
	v_rcp_f32_e32 v114, v114
	v_exp_f32_e32 v111, v111
	v_pk_fma_f32 v[106:107], v[106:107], s[20:21], v[238:239] op_sel_hi:[1,0,1]
	v_mul_f32_e32 v110, v110, v114
	v_min_f32_e32 v106, 0x40e00000, v106
	v_fma_f32 v109, v109, v110, v110
	v_add_f32_e32 v110, 1.0, v111
	v_mul_f32_e32 v111, 0xc01d265f, v106
	v_rcp_f32_e32 v110, v110
	v_exp_f32_e32 v111, v111
	v_med3_f32 v105, v105, s61, v172
	v_mul_f32_e32 v104, v104, v110
	v_fma_f32 v104, v105, v104, v104
	v_add_f32_e32 v105, 1.0, v111
	v_rcp_f32_e32 v105, v105
	v_cvt_pk_fp8_f32 v202, v108, v109
	v_med3_f32 v107, v107, s61, v172
	v_mul_f32_e32 v105, v106, v105
	v_pk_fma_f32 v[100:101], v[100:101], s[20:21], v[240:241] op_sel_hi:[1,0,1]
	v_fma_f32 v105, v107, v105, v105
	v_min_f32_e32 v100, 0x40e00000, v100
	v_cvt_pk_fp8_f32 v202, v104, v105 op_sel:[0,0,1]
	v_mul_f32_e32 v104, 0xc01d265f, v100
	v_exp_f32_e32 v106, v104
	v_pk_fma_f32 v[102:103], v[102:103], s[20:21], v[242:243] op_sel_hi:[1,0,1]
	v_pk_fma_f32 v[96:97], v[96:97], s[20:21], v[244:245] op_sel_hi:[1,0,1]
	v_min_f32_e32 v102, 0x40e00000, v102
	v_add_f32_e32 v106, 1.0, v106
	v_mul_f32_e32 v107, 0xc01d265f, v102
	v_rcp_f32_e32 v106, v106
	v_exp_f32_e32 v107, v107
	v_med3_f32 v101, v101, s61, v172
	v_mul_f32_e32 v100, v100, v106
	v_min_f32_e32 v96, 0x40e00000, v96
	v_add_f32_e32 v106, 1.0, v107
	v_fma_f32 v100, v101, v100, v100
	v_med3_f32 v101, v103, s61, v172
	v_mul_f32_e32 v103, 0xc01d265f, v96
	v_rcp_f32_e32 v106, v106
	v_exp_f32_e32 v103, v103
	v_pk_fma_f32 v[98:99], v[98:99], s[20:21], v[246:247] op_sel_hi:[1,0,1]
	v_mul_f32_e32 v102, v102, v106
	v_min_f32_e32 v98, 0x40e00000, v98
	v_fma_f32 v101, v101, v102, v102
	v_add_f32_e32 v102, 1.0, v103
	v_mul_f32_e32 v103, 0xc01d265f, v98
	v_rcp_f32_e32 v102, v102
	v_exp_f32_e32 v103, v103
	v_med3_f32 v97, v97, s61, v172
	v_mul_f32_e32 v96, v96, v102
	v_fma_f32 v96, v97, v96, v96
	v_add_f32_e32 v97, 1.0, v103
	v_rcp_f32_e32 v97, v97
	v_cvt_pk_fp8_f32 v203, v100, v101
	v_med3_f32 v99, v99, s61, v172
	v_mul_f32_e32 v97, v98, v97
	v_fma_f32 v97, v99, v97, v97
	v_cvt_pk_fp8_f32 v203, v96, v97 op_sel:[0,0,1]
	v_lshlrev_b64 v[112:113], 11, v[144:145]
	v_lshl_add_u64 v[112:113], s[16:17], 0, v[112:113]
	v_lshl_add_u64 v[104:105], v[112:113], 0, v[150:151]
	global_store_dwordx2 v[104:105], v[202:203], off
.LBB0_1164:
	s_or_b64 exec, exec, s[10:11]
	v_add_u32_e32 v96, s39, v163
	v_cmp_gt_i32_e32 vcc, s38, v163
	s_nop 1
	v_cndmask_b32_e32 v144, -1, v96, vcc
	v_cmp_lt_i32_e32 vcc, -1, v144
	s_and_saveexec_b64 s[10:11], vcc
	s_cbranch_execz .LBB0_1166
	v_pk_fma_f32 v[92:93], v[92:93], s[20:21], v[232:233] op_sel_hi:[1,0,1]
	v_pk_fma_f32 v[94:95], v[94:95], s[20:21], v[234:235] op_sel_hi:[1,0,1]
	v_min_f32_e32 v92, 0x40e00000, v92
	v_mul_f32_e32 v98, 0xc01d265f, v92
	v_exp_f32_e32 v98, v98
	v_min_f32_e32 v94, 0x40e00000, v94
	v_mul_f32_e32 v99, 0xc01d265f, v94
	v_add_f32_e32 v98, 1.0, v98
	v_rcp_f32_e32 v98, v98
	v_exp_f32_e32 v99, v99
	v_pk_fma_f32 v[88:89], v[88:89], s[20:21], v[236:237] op_sel_hi:[1,0,1]
	v_med3_f32 v93, v93, s61, v172
	v_mul_f32_e32 v92, v92, v98
	v_min_f32_e32 v88, 0x40e00000, v88
	v_add_f32_e32 v98, 1.0, v99
	v_fma_f32 v92, v93, v92, v92
	v_med3_f32 v93, v95, s61, v172
	v_mul_f32_e32 v95, 0xc01d265f, v88
	v_rcp_f32_e32 v98, v98
	v_exp_f32_e32 v95, v95
	v_pk_fma_f32 v[90:91], v[90:91], s[20:21], v[238:239] op_sel_hi:[1,0,1]
	v_mul_f32_e32 v94, v94, v98
	v_min_f32_e32 v90, 0x40e00000, v90
	v_fma_f32 v93, v93, v94, v94
	v_add_f32_e32 v94, 1.0, v95
	v_mul_f32_e32 v95, 0xc01d265f, v90
	v_rcp_f32_e32 v94, v94
	v_exp_f32_e32 v95, v95
	v_med3_f32 v89, v89, s61, v172
	v_mul_f32_e32 v88, v88, v94
	v_fma_f32 v88, v89, v88, v88
	v_add_f32_e32 v89, 1.0, v95
	v_rcp_f32_e32 v89, v89
	v_cvt_pk_fp8_f32 v204, v92, v93
	v_med3_f32 v91, v91, s61, v172
	v_mul_f32_e32 v89, v90, v89
	v_pk_fma_f32 v[84:85], v[84:85], s[20:21], v[240:241] op_sel_hi:[1,0,1]
	v_fma_f32 v89, v91, v89, v89
	v_min_f32_e32 v84, 0x40e00000, v84
	v_cvt_pk_fp8_f32 v204, v88, v89 op_sel:[0,0,1]
	v_mul_f32_e32 v88, 0xc01d265f, v84
	v_exp_f32_e32 v90, v88
	v_pk_fma_f32 v[86:87], v[86:87], s[20:21], v[242:243] op_sel_hi:[1,0,1]
	v_pk_fma_f32 v[80:81], v[80:81], s[20:21], v[244:245] op_sel_hi:[1,0,1]
	v_min_f32_e32 v86, 0x40e00000, v86
	v_add_f32_e32 v90, 1.0, v90
	v_mul_f32_e32 v91, 0xc01d265f, v86
	v_rcp_f32_e32 v90, v90
	v_exp_f32_e32 v91, v91
	v_med3_f32 v85, v85, s61, v172
	v_mul_f32_e32 v84, v84, v90
	v_min_f32_e32 v80, 0x40e00000, v80
	v_add_f32_e32 v90, 1.0, v91
	v_fma_f32 v84, v85, v84, v84
	v_med3_f32 v85, v87, s61, v172
	v_mul_f32_e32 v87, 0xc01d265f, v80
	v_rcp_f32_e32 v90, v90
	v_exp_f32_e32 v87, v87
	v_pk_fma_f32 v[82:83], v[82:83], s[20:21], v[246:247] op_sel_hi:[1,0,1]
	v_mul_f32_e32 v86, v86, v90
	v_min_f32_e32 v82, 0x40e00000, v82
	v_fma_f32 v85, v85, v86, v86
	v_add_f32_e32 v86, 1.0, v87
	v_mul_f32_e32 v87, 0xc01d265f, v82
	v_rcp_f32_e32 v86, v86
	v_exp_f32_e32 v87, v87
	v_med3_f32 v81, v81, s61, v172
	v_mul_f32_e32 v80, v80, v86
	v_fma_f32 v80, v81, v80, v80
	v_add_f32_e32 v81, 1.0, v87
	v_rcp_f32_e32 v81, v81
	v_cvt_pk_fp8_f32 v205, v84, v85
	v_med3_f32 v83, v83, s61, v172
	v_mul_f32_e32 v81, v82, v81
	v_fma_f32 v81, v83, v81, v81
	v_cvt_pk_fp8_f32 v205, v80, v81 op_sel:[0,0,1]
	v_lshlrev_b64 v[96:97], 11, v[144:145]
	v_lshl_add_u64 v[96:97], s[16:17], 0, v[96:97]
	v_lshl_add_u64 v[88:89], v[96:97], 0, v[150:151]
	global_store_dwordx2 v[88:89], v[204:205], off
.LBB0_1166:
	s_or_b64 exec, exec, s[10:11]
	v_add_u32_e32 v80, s39, v164
	v_cmp_gt_i32_e32 vcc, s38, v164
	s_nop 1
	v_cndmask_b32_e32 v144, -1, v80, vcc
	v_cmp_lt_i32_e32 vcc, -1, v144
	s_and_saveexec_b64 s[10:11], vcc
	s_cbranch_execz .LBB0_1168
	v_pk_fma_f32 v[76:77], v[76:77], s[20:21], v[232:233] op_sel_hi:[1,0,1]
	v_pk_fma_f32 v[78:79], v[78:79], s[20:21], v[234:235] op_sel_hi:[1,0,1]
	v_min_f32_e32 v76, 0x40e00000, v76
	v_mul_f32_e32 v82, 0xc01d265f, v76
	v_exp_f32_e32 v82, v82
	v_min_f32_e32 v78, 0x40e00000, v78
	v_mul_f32_e32 v83, 0xc01d265f, v78
	v_add_f32_e32 v82, 1.0, v82
	v_rcp_f32_e32 v82, v82
	v_exp_f32_e32 v83, v83
	v_pk_fma_f32 v[72:73], v[72:73], s[20:21], v[236:237] op_sel_hi:[1,0,1]
	v_med3_f32 v77, v77, s61, v172
	v_mul_f32_e32 v76, v76, v82
	v_min_f32_e32 v72, 0x40e00000, v72
	v_add_f32_e32 v82, 1.0, v83
	v_fma_f32 v76, v77, v76, v76
	v_med3_f32 v77, v79, s61, v172
	v_mul_f32_e32 v79, 0xc01d265f, v72
	v_rcp_f32_e32 v82, v82
	v_exp_f32_e32 v79, v79
	v_pk_fma_f32 v[74:75], v[74:75], s[20:21], v[238:239] op_sel_hi:[1,0,1]
	v_mul_f32_e32 v78, v78, v82
	v_min_f32_e32 v74, 0x40e00000, v74
	v_fma_f32 v77, v77, v78, v78
	v_add_f32_e32 v78, 1.0, v79
	v_mul_f32_e32 v79, 0xc01d265f, v74
	v_rcp_f32_e32 v78, v78
	v_exp_f32_e32 v79, v79
	v_med3_f32 v73, v73, s61, v172
	v_mul_f32_e32 v72, v72, v78
	v_fma_f32 v72, v73, v72, v72
	v_add_f32_e32 v73, 1.0, v79
	v_rcp_f32_e32 v73, v73
	v_cvt_pk_fp8_f32 v206, v76, v77
	v_med3_f32 v75, v75, s61, v172
	v_mul_f32_e32 v73, v74, v73
	v_pk_fma_f32 v[68:69], v[68:69], s[20:21], v[240:241] op_sel_hi:[1,0,1]
	v_fma_f32 v73, v75, v73, v73
	v_min_f32_e32 v68, 0x40e00000, v68
	v_cvt_pk_fp8_f32 v206, v72, v73 op_sel:[0,0,1]
	v_mul_f32_e32 v72, 0xc01d265f, v68
	v_exp_f32_e32 v74, v72
	v_pk_fma_f32 v[70:71], v[70:71], s[20:21], v[242:243] op_sel_hi:[1,0,1]
	v_pk_fma_f32 v[64:65], v[64:65], s[20:21], v[244:245] op_sel_hi:[1,0,1]
	v_min_f32_e32 v70, 0x40e00000, v70
	v_add_f32_e32 v74, 1.0, v74
	v_mul_f32_e32 v75, 0xc01d265f, v70
	v_rcp_f32_e32 v74, v74
	v_exp_f32_e32 v75, v75
	v_med3_f32 v69, v69, s61, v172
	v_mul_f32_e32 v68, v68, v74
	v_min_f32_e32 v64, 0x40e00000, v64
	v_add_f32_e32 v74, 1.0, v75
	v_fma_f32 v68, v69, v68, v68
	v_med3_f32 v69, v71, s61, v172
	v_mul_f32_e32 v71, 0xc01d265f, v64
	v_rcp_f32_e32 v74, v74
	v_exp_f32_e32 v71, v71
	v_pk_fma_f32 v[66:67], v[66:67], s[20:21], v[246:247] op_sel_hi:[1,0,1]
	v_mul_f32_e32 v70, v70, v74
	v_min_f32_e32 v66, 0x40e00000, v66
	v_fma_f32 v69, v69, v70, v70
	v_add_f32_e32 v70, 1.0, v71
	v_mul_f32_e32 v71, 0xc01d265f, v66
	v_rcp_f32_e32 v70, v70
	v_exp_f32_e32 v71, v71
	v_med3_f32 v65, v65, s61, v172
	v_mul_f32_e32 v64, v64, v70
	v_fma_f32 v64, v65, v64, v64
	v_add_f32_e32 v65, 1.0, v71
	v_rcp_f32_e32 v65, v65
	v_cvt_pk_fp8_f32 v207, v68, v69
	v_med3_f32 v67, v67, s61, v172
	v_mul_f32_e32 v65, v66, v65
	v_fma_f32 v65, v67, v65, v65
	v_cvt_pk_fp8_f32 v207, v64, v65 op_sel:[0,0,1]
	v_lshlrev_b64 v[80:81], 11, v[144:145]
	v_lshl_add_u64 v[80:81], s[16:17], 0, v[80:81]
	v_lshl_add_u64 v[72:73], v[80:81], 0, v[150:151]
	global_store_dwordx2 v[72:73], v[206:207], off
.LBB0_1168:
	s_or_b64 exec, exec, s[10:11]
	v_add_u32_e32 v64, s39, v165
	v_cmp_gt_i32_e32 vcc, s38, v165
	s_nop 1
	v_cndmask_b32_e32 v144, -1, v64, vcc
	v_cmp_lt_i32_e32 vcc, -1, v144
	s_and_saveexec_b64 s[10:11], vcc
	s_cbranch_execz .LBB0_1170
	v_pk_fma_f32 v[60:61], v[60:61], s[20:21], v[232:233] op_sel_hi:[1,0,1]
	v_pk_fma_f32 v[62:63], v[62:63], s[20:21], v[234:235] op_sel_hi:[1,0,1]
	v_min_f32_e32 v60, 0x40e00000, v60
	v_mul_f32_e32 v66, 0xc01d265f, v60
	v_exp_f32_e32 v66, v66
	v_min_f32_e32 v62, 0x40e00000, v62
	v_mul_f32_e32 v67, 0xc01d265f, v62
	v_add_f32_e32 v66, 1.0, v66
	v_rcp_f32_e32 v66, v66
	v_exp_f32_e32 v67, v67
	v_pk_fma_f32 v[56:57], v[56:57], s[20:21], v[236:237] op_sel_hi:[1,0,1]
	v_med3_f32 v61, v61, s61, v172
	v_mul_f32_e32 v60, v60, v66
	v_min_f32_e32 v56, 0x40e00000, v56
	v_add_f32_e32 v66, 1.0, v67
	v_fma_f32 v60, v61, v60, v60
	v_med3_f32 v61, v63, s61, v172
	v_mul_f32_e32 v63, 0xc01d265f, v56
	v_rcp_f32_e32 v66, v66
	v_exp_f32_e32 v63, v63
	v_pk_fma_f32 v[58:59], v[58:59], s[20:21], v[238:239] op_sel_hi:[1,0,1]
	v_mul_f32_e32 v62, v62, v66
	v_min_f32_e32 v58, 0x40e00000, v58
	v_fma_f32 v61, v61, v62, v62
	v_add_f32_e32 v62, 1.0, v63
	v_mul_f32_e32 v63, 0xc01d265f, v58
	v_rcp_f32_e32 v62, v62
	v_exp_f32_e32 v63, v63
	v_med3_f32 v57, v57, s61, v172
	v_mul_f32_e32 v56, v56, v62
	v_fma_f32 v56, v57, v56, v56
	v_add_f32_e32 v57, 1.0, v63
	v_rcp_f32_e32 v57, v57
	v_cvt_pk_fp8_f32 v208, v60, v61
	v_med3_f32 v59, v59, s61, v172
	v_mul_f32_e32 v57, v58, v57
	v_pk_fma_f32 v[52:53], v[52:53], s[20:21], v[240:241] op_sel_hi:[1,0,1]
	v_fma_f32 v57, v59, v57, v57
	v_min_f32_e32 v52, 0x40e00000, v52
	v_cvt_pk_fp8_f32 v208, v56, v57 op_sel:[0,0,1]
	v_mul_f32_e32 v56, 0xc01d265f, v52
	v_exp_f32_e32 v58, v56
	v_pk_fma_f32 v[54:55], v[54:55], s[20:21], v[242:243] op_sel_hi:[1,0,1]
	v_pk_fma_f32 v[48:49], v[48:49], s[20:21], v[244:245] op_sel_hi:[1,0,1]
	v_min_f32_e32 v54, 0x40e00000, v54
	v_add_f32_e32 v58, 1.0, v58
	v_mul_f32_e32 v59, 0xc01d265f, v54
	v_rcp_f32_e32 v58, v58
	v_exp_f32_e32 v59, v59
	v_med3_f32 v53, v53, s61, v172
	v_mul_f32_e32 v52, v52, v58
	v_min_f32_e32 v48, 0x40e00000, v48
	v_add_f32_e32 v58, 1.0, v59
	v_fma_f32 v52, v53, v52, v52
	v_med3_f32 v53, v55, s61, v172
	v_mul_f32_e32 v55, 0xc01d265f, v48
	v_rcp_f32_e32 v58, v58
	v_exp_f32_e32 v55, v55
	v_pk_fma_f32 v[50:51], v[50:51], s[20:21], v[246:247] op_sel_hi:[1,0,1]
	v_mul_f32_e32 v54, v54, v58
	v_min_f32_e32 v50, 0x40e00000, v50
	v_fma_f32 v53, v53, v54, v54
	v_add_f32_e32 v54, 1.0, v55
	v_mul_f32_e32 v55, 0xc01d265f, v50
	v_rcp_f32_e32 v54, v54
	v_exp_f32_e32 v55, v55
	v_med3_f32 v49, v49, s61, v172
	v_mul_f32_e32 v48, v48, v54
	v_fma_f32 v48, v49, v48, v48
	v_add_f32_e32 v49, 1.0, v55
	v_rcp_f32_e32 v49, v49
	v_cvt_pk_fp8_f32 v209, v52, v53
	v_med3_f32 v51, v51, s61, v172
	v_mul_f32_e32 v49, v50, v49
	v_fma_f32 v49, v51, v49, v49
	v_cvt_pk_fp8_f32 v209, v48, v49 op_sel:[0,0,1]
	v_lshlrev_b64 v[64:65], 11, v[144:145]
	v_lshl_add_u64 v[64:65], s[16:17], 0, v[64:65]
	v_lshl_add_u64 v[56:57], v[64:65], 0, v[150:151]
	global_store_dwordx2 v[56:57], v[208:209], off
.LBB0_1170:
	s_or_b64 exec, exec, s[10:11]
	v_add_u32_e32 v48, s39, v166
	v_cmp_gt_i32_e32 vcc, s38, v166
	s_nop 1
	v_cndmask_b32_e32 v144, -1, v48, vcc
	v_cmp_lt_i32_e32 vcc, -1, v144
	s_and_saveexec_b64 s[10:11], vcc
	s_cbranch_execz .LBB0_1172
	v_pk_fma_f32 v[44:45], v[44:45], s[20:21], v[232:233] op_sel_hi:[1,0,1]
	v_pk_fma_f32 v[46:47], v[46:47], s[20:21], v[234:235] op_sel_hi:[1,0,1]
	v_min_f32_e32 v44, 0x40e00000, v44
	v_mul_f32_e32 v50, 0xc01d265f, v44
	v_exp_f32_e32 v50, v50
	v_min_f32_e32 v46, 0x40e00000, v46
	v_mul_f32_e32 v51, 0xc01d265f, v46
	v_add_f32_e32 v50, 1.0, v50
	v_rcp_f32_e32 v50, v50
	v_exp_f32_e32 v51, v51
	v_pk_fma_f32 v[40:41], v[40:41], s[20:21], v[236:237] op_sel_hi:[1,0,1]
	v_med3_f32 v45, v45, s61, v172
	v_mul_f32_e32 v44, v44, v50
	v_min_f32_e32 v40, 0x40e00000, v40
	v_add_f32_e32 v50, 1.0, v51
	v_fma_f32 v44, v45, v44, v44
	v_med3_f32 v45, v47, s61, v172
	v_mul_f32_e32 v47, 0xc01d265f, v40
	v_rcp_f32_e32 v50, v50
	v_exp_f32_e32 v47, v47
	v_pk_fma_f32 v[42:43], v[42:43], s[20:21], v[238:239] op_sel_hi:[1,0,1]
	v_mul_f32_e32 v46, v46, v50
	v_min_f32_e32 v42, 0x40e00000, v42
	v_fma_f32 v45, v45, v46, v46
	v_add_f32_e32 v46, 1.0, v47
	v_mul_f32_e32 v47, 0xc01d265f, v42
	v_rcp_f32_e32 v46, v46
	v_exp_f32_e32 v47, v47
	v_med3_f32 v41, v41, s61, v172
	v_mul_f32_e32 v40, v40, v46
	v_fma_f32 v40, v41, v40, v40
	v_add_f32_e32 v41, 1.0, v47
	v_rcp_f32_e32 v41, v41
	v_cvt_pk_fp8_f32 v210, v44, v45
	v_med3_f32 v43, v43, s61, v172
	v_mul_f32_e32 v41, v42, v41
	v_pk_fma_f32 v[36:37], v[36:37], s[20:21], v[240:241] op_sel_hi:[1,0,1]
	v_fma_f32 v41, v43, v41, v41
	v_min_f32_e32 v36, 0x40e00000, v36
	v_cvt_pk_fp8_f32 v210, v40, v41 op_sel:[0,0,1]
	v_mul_f32_e32 v40, 0xc01d265f, v36
	v_exp_f32_e32 v42, v40
	v_pk_fma_f32 v[38:39], v[38:39], s[20:21], v[242:243] op_sel_hi:[1,0,1]
	v_pk_fma_f32 v[32:33], v[32:33], s[20:21], v[244:245] op_sel_hi:[1,0,1]
	v_min_f32_e32 v38, 0x40e00000, v38
	v_add_f32_e32 v42, 1.0, v42
	v_mul_f32_e32 v43, 0xc01d265f, v38
	v_rcp_f32_e32 v42, v42
	v_exp_f32_e32 v43, v43
	v_med3_f32 v37, v37, s61, v172
	v_mul_f32_e32 v36, v36, v42
	v_min_f32_e32 v32, 0x40e00000, v32
	v_add_f32_e32 v42, 1.0, v43
	v_fma_f32 v36, v37, v36, v36
	v_med3_f32 v37, v39, s61, v172
	v_mul_f32_e32 v39, 0xc01d265f, v32
	v_rcp_f32_e32 v42, v42
	v_exp_f32_e32 v39, v39
	v_pk_fma_f32 v[34:35], v[34:35], s[20:21], v[246:247] op_sel_hi:[1,0,1]
	v_mul_f32_e32 v38, v38, v42
	v_min_f32_e32 v34, 0x40e00000, v34
	v_fma_f32 v37, v37, v38, v38
	v_add_f32_e32 v38, 1.0, v39
	v_mul_f32_e32 v39, 0xc01d265f, v34
	v_rcp_f32_e32 v38, v38
	v_exp_f32_e32 v39, v39
	v_med3_f32 v33, v33, s61, v172
	v_mul_f32_e32 v32, v32, v38
	v_fma_f32 v32, v33, v32, v32
	v_add_f32_e32 v33, 1.0, v39
	v_rcp_f32_e32 v33, v33
	v_cvt_pk_fp8_f32 v211, v36, v37
	v_med3_f32 v35, v35, s61, v172
	v_mul_f32_e32 v33, v34, v33
	v_fma_f32 v33, v35, v33, v33
	v_cvt_pk_fp8_f32 v211, v32, v33 op_sel:[0,0,1]
	v_lshlrev_b64 v[48:49], 11, v[144:145]
	v_lshl_add_u64 v[48:49], s[16:17], 0, v[48:49]
	v_lshl_add_u64 v[40:41], v[48:49], 0, v[150:151]
	global_store_dwordx2 v[40:41], v[210:211], off
.LBB0_1172:
	s_or_b64 exec, exec, s[10:11]
	v_add_u32_e32 v32, s39, v167
	v_cmp_gt_i32_e32 vcc, s38, v167
	s_nop 1
	v_cndmask_b32_e32 v144, -1, v32, vcc
	v_cmp_lt_i32_e32 vcc, -1, v144
	s_and_saveexec_b64 s[10:11], vcc
	s_cbranch_execz .LBB0_1174
	v_pk_fma_f32 v[28:29], v[28:29], s[20:21], v[232:233] op_sel_hi:[1,0,1]
	v_pk_fma_f32 v[30:31], v[30:31], s[20:21], v[234:235] op_sel_hi:[1,0,1]
	v_min_f32_e32 v28, 0x40e00000, v28
	v_mul_f32_e32 v34, 0xc01d265f, v28
	v_exp_f32_e32 v34, v34
	v_min_f32_e32 v30, 0x40e00000, v30
	v_mul_f32_e32 v35, 0xc01d265f, v30
	v_add_f32_e32 v34, 1.0, v34
	v_rcp_f32_e32 v34, v34
	v_exp_f32_e32 v35, v35
	v_pk_fma_f32 v[24:25], v[24:25], s[20:21], v[236:237] op_sel_hi:[1,0,1]
	v_med3_f32 v29, v29, s61, v172
	v_mul_f32_e32 v28, v28, v34
	v_min_f32_e32 v24, 0x40e00000, v24
	v_add_f32_e32 v34, 1.0, v35
	v_fma_f32 v28, v29, v28, v28
	v_med3_f32 v29, v31, s61, v172
	v_mul_f32_e32 v31, 0xc01d265f, v24
	v_rcp_f32_e32 v34, v34
	v_exp_f32_e32 v31, v31
	v_pk_fma_f32 v[26:27], v[26:27], s[20:21], v[238:239] op_sel_hi:[1,0,1]
	v_mul_f32_e32 v30, v30, v34
	v_min_f32_e32 v26, 0x40e00000, v26
	v_fma_f32 v29, v29, v30, v30
	v_add_f32_e32 v30, 1.0, v31
	v_mul_f32_e32 v31, 0xc01d265f, v26
	v_rcp_f32_e32 v30, v30
	v_exp_f32_e32 v31, v31
	v_med3_f32 v25, v25, s61, v172
	v_mul_f32_e32 v24, v24, v30
	v_fma_f32 v24, v25, v24, v24
	v_add_f32_e32 v25, 1.0, v31
	v_rcp_f32_e32 v25, v25
	v_cvt_pk_fp8_f32 v212, v28, v29
	v_med3_f32 v27, v27, s61, v172
	v_mul_f32_e32 v25, v26, v25
	v_pk_fma_f32 v[20:21], v[20:21], s[20:21], v[240:241] op_sel_hi:[1,0,1]
	v_fma_f32 v25, v27, v25, v25
	v_min_f32_e32 v20, 0x40e00000, v20
	v_cvt_pk_fp8_f32 v212, v24, v25 op_sel:[0,0,1]
	v_mul_f32_e32 v24, 0xc01d265f, v20
	v_exp_f32_e32 v26, v24
	v_pk_fma_f32 v[22:23], v[22:23], s[20:21], v[242:243] op_sel_hi:[1,0,1]
	v_pk_fma_f32 v[16:17], v[16:17], s[20:21], v[244:245] op_sel_hi:[1,0,1]
	v_min_f32_e32 v22, 0x40e00000, v22
	v_add_f32_e32 v26, 1.0, v26
	v_mul_f32_e32 v27, 0xc01d265f, v22
	v_rcp_f32_e32 v26, v26
	v_exp_f32_e32 v27, v27
	v_med3_f32 v21, v21, s61, v172
	v_mul_f32_e32 v20, v20, v26
	v_min_f32_e32 v16, 0x40e00000, v16
	v_add_f32_e32 v26, 1.0, v27
	v_fma_f32 v20, v21, v20, v20
	v_med3_f32 v21, v23, s61, v172
	v_mul_f32_e32 v23, 0xc01d265f, v16
	v_rcp_f32_e32 v26, v26
	v_exp_f32_e32 v23, v23
	v_pk_fma_f32 v[18:19], v[18:19], s[20:21], v[246:247] op_sel_hi:[1,0,1]
	v_mul_f32_e32 v22, v22, v26
	v_min_f32_e32 v18, 0x40e00000, v18
	v_fma_f32 v21, v21, v22, v22
	v_add_f32_e32 v22, 1.0, v23
	v_mul_f32_e32 v23, 0xc01d265f, v18
	v_rcp_f32_e32 v22, v22
	v_exp_f32_e32 v23, v23
	v_med3_f32 v17, v17, s61, v172
	v_mul_f32_e32 v16, v16, v22
	v_fma_f32 v16, v17, v16, v16
	v_add_f32_e32 v17, 1.0, v23
	v_rcp_f32_e32 v17, v17
	v_cvt_pk_fp8_f32 v213, v20, v21
	v_med3_f32 v19, v19, s61, v172
	v_mul_f32_e32 v17, v18, v17
	v_fma_f32 v17, v19, v17, v17
	v_cvt_pk_fp8_f32 v213, v16, v17 op_sel:[0,0,1]
	v_lshlrev_b64 v[32:33], 11, v[144:145]
	v_lshl_add_u64 v[32:33], s[16:17], 0, v[32:33]
	v_lshl_add_u64 v[24:25], v[32:33], 0, v[150:151]
	global_store_dwordx2 v[24:25], v[212:213], off
.LBB0_1174:
	s_or_b64 exec, exec, s[10:11]
	v_add_u32_e32 v16, s39, v168
	v_cmp_gt_i32_e32 vcc, s38, v168
	s_nop 1
	v_cndmask_b32_e32 v144, -1, v16, vcc
	v_cmp_lt_i32_e32 vcc, -1, v144
	s_and_saveexec_b64 s[10:11], vcc
	s_cbranch_execz .LBB0_1176
	v_pk_fma_f32 v[12:13], v[12:13], s[20:21], v[232:233] op_sel_hi:[1,0,1]
	v_pk_fma_f32 v[14:15], v[14:15], s[20:21], v[234:235] op_sel_hi:[1,0,1]
	v_min_f32_e32 v12, 0x40e00000, v12
	v_mul_f32_e32 v18, 0xc01d265f, v12
	v_exp_f32_e32 v18, v18
	v_min_f32_e32 v14, 0x40e00000, v14
	v_mul_f32_e32 v19, 0xc01d265f, v14
	v_add_f32_e32 v18, 1.0, v18
	v_rcp_f32_e32 v18, v18
	v_exp_f32_e32 v19, v19
	v_pk_fma_f32 v[8:9], v[8:9], s[20:21], v[236:237] op_sel_hi:[1,0,1]
	v_med3_f32 v13, v13, s61, v172
	v_mul_f32_e32 v12, v12, v18
	v_min_f32_e32 v8, 0x40e00000, v8
	v_add_f32_e32 v18, 1.0, v19
	v_fma_f32 v12, v13, v12, v12
	v_med3_f32 v13, v15, s61, v172
	v_mul_f32_e32 v15, 0xc01d265f, v8
	v_rcp_f32_e32 v18, v18
	v_exp_f32_e32 v15, v15
	v_pk_fma_f32 v[10:11], v[10:11], s[20:21], v[238:239] op_sel_hi:[1,0,1]
	v_mul_f32_e32 v14, v14, v18
	v_min_f32_e32 v10, 0x40e00000, v10
	v_fma_f32 v13, v13, v14, v14
	v_add_f32_e32 v14, 1.0, v15
	v_mul_f32_e32 v15, 0xc01d265f, v10
	v_rcp_f32_e32 v14, v14
	v_exp_f32_e32 v15, v15
	v_med3_f32 v9, v9, s61, v172
	v_mul_f32_e32 v8, v8, v14
	v_fma_f32 v8, v9, v8, v8
	v_add_f32_e32 v9, 1.0, v15
	v_rcp_f32_e32 v9, v9
	v_cvt_pk_fp8_f32 v214, v12, v13
	v_med3_f32 v11, v11, s61, v172
	v_mul_f32_e32 v9, v10, v9
	v_pk_fma_f32 v[4:5], v[4:5], s[20:21], v[240:241] op_sel_hi:[1,0,1]
	v_fma_f32 v9, v11, v9, v9
	v_min_f32_e32 v4, 0x40e00000, v4
	v_cvt_pk_fp8_f32 v214, v8, v9 op_sel:[0,0,1]
	v_mul_f32_e32 v8, 0xc01d265f, v4
	v_exp_f32_e32 v10, v8
	v_pk_fma_f32 v[6:7], v[6:7], s[20:21], v[242:243] op_sel_hi:[1,0,1]
	v_pk_fma_f32 v[0:1], v[0:1], s[20:21], v[244:245] op_sel_hi:[1,0,1]
	v_min_f32_e32 v6, 0x40e00000, v6
	v_add_f32_e32 v10, 1.0, v10
	v_mul_f32_e32 v11, 0xc01d265f, v6
	v_rcp_f32_e32 v10, v10
	v_exp_f32_e32 v11, v11
	v_med3_f32 v5, v5, s61, v172
	v_mul_f32_e32 v4, v4, v10
	v_min_f32_e32 v0, 0x40e00000, v0
	v_add_f32_e32 v10, 1.0, v11
	v_fma_f32 v4, v5, v4, v4
	v_med3_f32 v5, v7, s61, v172
	v_mul_f32_e32 v7, 0xc01d265f, v0
	v_rcp_f32_e32 v10, v10
	v_exp_f32_e32 v7, v7
	v_pk_fma_f32 v[2:3], v[2:3], s[20:21], v[246:247] op_sel_hi:[1,0,1]
	v_mul_f32_e32 v6, v6, v10
	v_min_f32_e32 v2, 0x40e00000, v2
	v_fma_f32 v5, v5, v6, v6
	v_add_f32_e32 v6, 1.0, v7
	v_mul_f32_e32 v7, 0xc01d265f, v2
	v_rcp_f32_e32 v6, v6
	v_exp_f32_e32 v7, v7
	v_med3_f32 v1, v1, s61, v172
	v_mul_f32_e32 v0, v0, v6
	v_fma_f32 v0, v1, v0, v0
	v_add_f32_e32 v1, 1.0, v7
	v_rcp_f32_e32 v1, v1
	v_cvt_pk_fp8_f32 v215, v4, v5
	v_med3_f32 v3, v3, s61, v172
	v_mul_f32_e32 v1, v2, v1
	v_fma_f32 v1, v3, v1, v1
	v_cvt_pk_fp8_f32 v215, v0, v1 op_sel:[0,0,1]
	v_lshlrev_b64 v[16:17], 11, v[144:145]
	v_lshl_add_u64 v[16:17], s[16:17], 0, v[16:17]
	v_lshl_add_u64 v[8:9], v[16:17], 0, v[150:151]
	global_store_dwordx2 v[8:9], v[214:215], off
